# norm2 router dot products on 4x4x4 bf16 MFMA (lane-private diagonal) instead of v_dot2c
# speedup vs baseline: 1.0138x; 1.0027x over previous
; #define GAS __attribute__((address_space(1)))
; __device__ __forceinline__ f32x4 ld_bf4(const bf16* p) { const v2u w = *(const GAS v2u*)p; return (f32x4){bflo(w.x), bfhi(w.x), bflo(w.y), bfhi(w.y)}; }
; __device__ __forceinline__ float row_rs(const f32x4 (&x)[8]) {
;     float s = 0.f;
; #pragma unroll
;     for (int j = 0; j < 8; ++j) s += (x[j][0] * x[j][0] + x[j][1] * x[j][1]) + (x[j][2] * x[j][2] + x[j][3] * x[j][3]);
;     return 1.0f / sqrtf(wave_sum(s) * (1.0f / DM) + EPS);
; }
; __device__ __forceinline__ void phase_norm2(Frame& F, int l) {
;     ...
;         const int rb = r < ML ? (r >> 11) : 8; const bf16* xr = WSP(bf16, WS_XM) + (size_t)r * DM;
;         f32x4 x[8];
; #pragma unroll
;         for (int j = 0; j < 8; ++j) x[j] = ld_bf4(xr + j * 256 + 4 * F.lane);
;         if (rb != rb_cur) { rb_cur = rb; const float* sh = modl + (size_t)(rb * 6 + 3) * DM; const float* sc = modl + (size_t)(rb * 6 + 4) * DM;
; #pragma unroll
;             for (int j = 0; j < 8; ++j) { const int c = j * 256 + 4 * F.lane; ga[j] = *(const GAS f32x4*)(gn + c) * (1.0f + *(const GAS f32x4*)(sc + c)); sb[j] = *(const GAS f32x4*)(sh + c); } }
;         const float rs = row_rs(x);
;         unsigned char* ho = WSP(unsigned char, WS_H) + (size_t)r * DM;
; #pragma unroll
;         for (int j = 0; j < 8; ++j) { const int c = j * 256 + 4 * F.lane;
;             x[j] = x[j] * rs * ga[j] + sb[j]; *(GAS unsigned*)(ho + c) = pk4_fp8(x[j][0] * FP8_SH, x[j][1] * FP8_SH, x[j][2] * FP8_SH, x[j][3] * FP8_SH); }
.LBB0_918:
	s_nop 0
	v_and_b32_e32 v117, 0xffff0000, v96
	v_and_b32_e32 v116, 0xffff0000, v94
	v_and_b32_e32 v121, 0xffff0000, v97
	v_and_b32_e32 v120, 0xffff0000, v95
	v_lshlrev_b32_e32 v115, 16, v96
	v_lshlrev_b32_e32 v114, 16, v94
	v_lshlrev_b32_e32 v119, 16, v97
	v_lshlrev_b32_e32 v118, 16, v95
	v_pk_mul_f32 v[130:131], v[116:117], v[116:117]
	v_pk_mul_f32 v[132:133], v[120:121], v[120:121]
	s_nop 0
	v_and_b32_e32 v125, 0xffff0000, v93
	v_and_b32_e32 v124, 0xffff0000, v92
	v_pk_fma_f32 v[130:131], v[114:115], v[114:115], v[130:131]
	v_pk_fma_f32 v[132:133], v[118:119], v[118:119], v[132:133]
	v_lshlrev_b32_e32 v123, 16, v93
	v_lshlrev_b32_e32 v122, 16, v92
	s_nop 0
	v_lshlrev_b32_e32 v126, 16, v90
	v_and_b32_e32 v127, 0xffff0000, v90
	v_lshlrev_b32_e32 v128, 16, v91
	s_nop 0
	v_lshlrev_b32_e32 v96, 16, v88
	v_pk_add_f32 v[130:131], v[130:131], v[132:133]
	v_pk_mul_f32 v[132:133], v[124:125], v[124:125]
	v_and_b32_e32 v129, 0xffff0000, v91
	v_pk_fma_f32 v[132:133], v[122:123], v[122:123], v[132:133]
	v_mul_f32_e32 v97, v126, v126
	v_mul_f32_e32 v135, v127, v127
	v_mul_f32_e32 v66, v128, v128
	v_mov_b32_e32 v134, v96
	v_and_b32_e32 v113, 0xffff0000, v88
	v_lshlrev_b32_e32 v94, 16, v89
	v_and_b32_e32 v95, 0xffff0000, v89
	v_pk_add_f32 v[130:131], v[130:131], v[130:131] op_sel_hi:[0,1]
	v_pk_add_f32 v[132:133], v[132:133], v[132:133] op_sel_hi:[0,1]
	v_pk_fma_f32 v[136:137], v[128:129], v[128:129], v[66:67] op_sel_hi:[1,1,0]
	v_pk_add_f32 v[134:135], v[96:97], v[134:135]
	s_nop 0
	v_and_b32_e32 v91, 0xffff0000, v87
	v_and_b32_e32 v90, 0xffff0000, v86
	v_mul_f32_e32 v136, v113, v113
	v_mul_f32_e32 v132, v94, v94
	v_mul_f32_e32 v130, v95, v95
	v_mul_f32_e32 v138, v96, v96
	v_mov_b32_e32 v139, v135
	v_lshlrev_b32_e32 v93, 16, v87
	v_lshlrev_b32_e32 v92, 16, v86
	s_nop 0
	v_lshlrev_b32_e32 v86, 16, v84
	v_and_b32_e32 v87, 0xffff0000, v84
	v_lshlrev_b32_e32 v88, 16, v85
	s_nop 0
	v_lshlrev_b32_e32 v84, 16, v82
	v_pk_add_f32 v[134:135], v[138:139], v[136:137]
	v_pk_add_f32 v[130:131], v[132:133], v[130:131]
	v_pk_mul_f32 v[132:133], v[90:91], v[90:91]
	v_and_b32_e32 v89, 0xffff0000, v85
	v_pk_add_f32 v[130:131], v[134:135], v[130:131]
	v_pk_fma_f32 v[132:133], v[92:93], v[92:93], v[132:133]
	v_mul_f32_e32 v85, v86, v86
	v_mul_f32_e32 v135, v87, v87
	v_mul_f32_e32 v66, v88, v88
	v_mov_b32_e32 v134, v84
	v_and_b32_e32 v146, 0xffff0000, v82
	v_lshlrev_b32_e32 v82, 16, v83
	v_and_b32_e32 v83, 0xffff0000, v83
	v_pk_add_f32 v[130:131], v[130:131], v[130:131] op_sel_hi:[0,1]
	v_pk_add_f32 v[132:133], v[132:133], v[132:133] op_sel_hi:[0,1]
	v_pk_fma_f32 v[136:137], v[88:89], v[88:89], v[66:67] op_sel_hi:[1,1,0]
	v_pk_add_f32 v[134:135], v[84:85], v[134:135]
	v_mul_f32_e32 v136, v146, v146
	v_mul_f32_e32 v132, v82, v82
	v_mul_f32_e32 v130, v83, v83
	v_mul_f32_e32 v138, v84, v84
	v_mov_b32_e32 v139, v135
	v_pk_add_f32 v[134:135], v[138:139], v[136:137]
	v_pk_add_f32 v[130:131], v[132:133], v[130:131]
	v_mov_b32_e32 v133, v120
	v_pk_add_f32 v[130:131], v[134:135], v[130:131]
	v_mov_b32_e32 v136, 0
	v_add_f32_e32 v66, v130, v131
	v_mov_b32_e32 v120, v119
	v_mov_b32_e32 v137, 0
	v_mov_b32_e32 v138, 0
	v_lshl_add_u64 v[134:135], s[2:3], 0, v[78:79]
	v_add_f32_dpp v85, v66, v66 quad_perm:[1,0,3,2] row_mask:0xf bank_mask:0xf
	s_nop 1
	v_add_f32_dpp v66, v85, v85 quad_perm:[2,3,0,1] row_mask:0xf bank_mask:0xf
	s_nop 1
	v_mov_b32_dpp v85, v66 row_half_mirror row_mask:0xf bank_mask:0xf
	s_nop 1
	v_add_f32_dpp v66, v85, v66 quad_perm:[3,2,1,0] row_mask:0xf bank_mask:0xf
	s_nop 1
	v_add_f32_dpp v85, v66, v66 row_ror:8 row_mask:0xf bank_mask:0xf
	v_mov_b32_e32 v66, v85
	s_nop 1
	v_permlane16_swap_b32_e32 v85, v66
	v_add_f32_e32 v66, v85, v66
	v_mov_b32_e32 v85, v66
	s_nop 1
	v_permlane32_swap_b32_e32 v66, v85
	v_add_f32_e32 v66, v66, v85
	v_fmamk_f32 v66, v66, 0x3a000000, v110
	v_mul_f32_e32 v85, 0x4f800000, v66
	v_cmp_gt_f32_e32 vcc, s17, v66
	s_nop 1
	v_cndmask_b32_e32 v66, v66, v85, vcc
	v_sqrt_f32_e32 v85, v66
	s_nop 0
	v_add_u32_e32 v97, -1, v85
	v_fma_f32 v130, -v97, v85, v66
	v_cmp_ge_f32_e64 s[14:15], 0, v130
	v_add_u32_e32 v130, 1, v85
	s_nop 0
	v_cndmask_b32_e64 v97, v85, v97, s[14:15]
	v_fma_f32 v85, -v130, v85, v66
	v_cmp_lt_f32_e64 s[14:15], 0, v85
	s_nop 1
	v_cndmask_b32_e64 v85, v97, v130, s[14:15]
	v_mul_f32_e32 v97, 0x37800000, v85
	v_cndmask_b32_e32 v85, v85, v97, vcc
	v_cmp_class_f32_e32 vcc, v66, v111
	s_nop 1
	v_cndmask_b32_e32 v66, v85, v66, vcc
	v_div_scale_f32 v85, s[0:1], v66, v66, 1.0
	v_rcp_f32_e32 v97, v85
	s_nop 0
	v_fma_f32 v130, -v85, v97, 1.0
	v_fmac_f32_e32 v97, v130, v97
	v_div_scale_f32 v130, vcc, 1.0, v66, 1.0
	v_mul_f32_e32 v131, v130, v97
	v_fma_f32 v132, -v85, v131, v130
	v_fmac_f32_e32 v131, v132, v97
	v_fma_f32 v85, -v85, v131, v130
	v_div_fmas_f32 v85, v85, v97, v131
	v_div_fixup_f32 v66, v85, v66, 1.0
	v_mov_b32_e32 v130, v114
	v_mov_b32_e32 v131, v116
	v_pk_mul_f32 v[130:131], v[130:131], v[66:67] op_sel_hi:[1,0]
	v_mov_b32_e32 v132, v118
	v_pk_fma_f32 v[130:131], v[34:35], v[130:131], v[2:3]
	v_pk_mul_f32 v[132:133], v[132:133], v[66:67] op_sel_hi:[1,0]
	v_mul_f32_e32 v85, 0x41800000, v130
	v_mul_f32_e32 v97, 0x41800000, v131
	v_med3_f32 v85, v85, s31, v112
	v_med3_f32 v97, v97, s31, v112
	v_pk_fma_f32 v[132:133], v[36:37], v[132:133], v[4:5]
	v_cvt_pk_fp8_f32 v136, v85, v97
	v_mul_f32_e32 v114, 0x41800000, v132
	v_mov_b32_e32 v116, v115
	v_mul_f32_e32 v85, 0x41800000, v133
	v_med3_f32 v97, v114, s31, v112
	v_pk_mul_f32 v[114:115], v[116:117], v[66:67] op_sel_hi:[1,0]
	v_med3_f32 v85, v85, s31, v112
	v_pk_fma_f32 v[118:119], v[38:39], v[114:115], v[6:7]
	v_cvt_pk_fp8_f32 v136, v97, v85 op_sel:[0,0,1]
; #define GAS __attribute__((address_space(1)))
; #define LAS __attribute__((address_space(3)))
; __device__ __forceinline__ unsigned cvt_pk_bf16(float lo, float hi) { unsigned r; asm volatile("v_cvt_pk_bf16_f32 %0, %1, %2" : "=v"(r) : "v"(lo), "v"(hi)); return r; }
; __device__ __forceinline__ void phase_norm2(Frame& F, int l) {
;     ...
;         for (int j = 0; j < 8; ++j) { const int c = j * 256 + 4 * F.lane;
;             x[j] = x[j] * rs * ga[j] + sb[j]; *(GAS unsigned*)(ho + c) = pk4_fp8(x[j][0] * FP8_SH, x[j][1] * FP8_SH, x[j][2] * FP8_SH, x[j][3] * FP8_SH); }
;         typedef __bf16 bf2_t __attribute__((ext_vector_type(2)));
;         unsigned xb[8][2];
; #pragma unroll
;         for (int j = 0; j < 8; ++j) { xb[j][0] = pg8::cvt_pk_bf16(x[j][0], x[j][1]); xb[j][1] = pg8::cvt_pk_bf16(x[j][2], x[j][3]); }
;     ...
;                 const v2u w0 = *(const LAS v2u*)(rwt + eg * DM + o), w1 = *(const LAS v2u*)(rwt + (eg + 1) * DM + o), w2 = *(const LAS v2u*)(rwt + (eg + 2) * DM + o), w3 = *(const LAS v2u*)(rwt + (eg + 3) * DM + o);
	v_pk_mul_f32 v[116:117], v[120:121], v[66:67] op_sel_hi:[1,0]
	v_mul_f32_e32 v85, 0x41800000, v118
	v_mul_f32_e32 v97, 0x41800000, v119
	v_pk_fma_f32 v[116:117], v[40:41], v[116:117], v[8:9]
	v_med3_f32 v85, v85, s31, v112
	v_med3_f32 v97, v97, s31, v112
	v_mul_f32_e32 v114, 0x41800000, v116
	v_cvt_pk_fp8_f32 v137, v85, v97
	v_med3_f32 v97, v114, s31, v112
	v_mov_b32_e32 v114, v122
	v_mov_b32_e32 v115, v124
	v_mul_f32_e32 v85, 0x41800000, v117
	v_pk_mul_f32 v[114:115], v[66:67], v[114:115] op_sel_hi:[0,1]
	v_med3_f32 v85, v85, s31, v112
	v_mov_b32_e32 v124, v123
	v_pk_fma_f32 v[122:123], v[42:43], v[114:115], v[10:11]
	v_cvt_pk_fp8_f32 v137, v97, v85 op_sel:[0,0,1]
	v_mul_f32_e32 v85, 0x41800000, v122
	v_mul_f32_e32 v97, 0x41800000, v123
	v_pk_mul_f32 v[120:121], v[66:67], v[124:125] op_sel_hi:[0,1]
	v_med3_f32 v85, v85, s31, v112
	v_med3_f32 v97, v97, s31, v112
	v_pk_fma_f32 v[120:121], v[44:45], v[120:121], v[12:13]
	v_cvt_pk_fp8_f32 v138, v85, v97
	v_mul_f32_e32 v114, 0x41800000, v120
	v_mul_f32_e32 v85, 0x41800000, v121
	v_med3_f32 v97, v114, s31, v112
	v_pk_mul_f32 v[114:115], v[126:127], v[66:67] op_sel_hi:[1,0]
	v_med3_f32 v85, v85, s31, v112
	v_pk_fma_f32 v[126:127], v[46:47], v[114:115], v[14:15]
	v_cvt_pk_fp8_f32 v138, v97, v85 op_sel:[0,0,1]
	v_mul_f32_e32 v85, 0x41800000, v126
	v_mul_f32_e32 v97, 0x41800000, v127
	v_med3_f32 v85, v85, s31, v112
	v_med3_f32 v97, v97, s31, v112
	v_mov_b32_e32 v115, 0
	v_pk_mul_f32 v[124:125], v[128:129], v[66:67] op_sel_hi:[1,0]
	v_cvt_pk_fp8_f32 v115, v85, v97
	v_pk_fma_f32 v[124:125], v[48:49], v[124:125], v[16:17]
	v_add_co_u32_e32 v134, vcc, s34, v134
	v_mul_f32_e32 v114, 0x41800000, v124
	v_mul_f32_e32 v85, 0x41800000, v125
	v_med3_f32 v97, v114, s31, v112
	v_med3_f32 v85, v85, s31, v112
	v_cvt_pk_fp8_f32 v115, v97, v85 op_sel:[0,0,1]
	v_mov_b32_e32 v97, v113
	v_addc_co_u32_e32 v135, vcc, 0, v135, vcc
	v_pk_mul_f32 v[96:97], v[96:97], v[66:67] op_sel_hi:[1,0]
	global_store_dword v[134:135], v136, off
	global_store_dword v[134:135], v137, off offset:256
	global_store_dword v[134:135], v138, off offset:512
	global_store_dword v[134:135], v115, off offset:768
	v_pk_mul_f32 v[94:95], v[94:95], v[66:67] op_sel_hi:[1,0]
	v_pk_fma_f32 v[136:137], v[50:51], v[96:97], v[18:19]
	v_pk_fma_f32 v[128:129], v[52:53], v[94:95], v[20:21]
	v_mul_f32_e32 v85, 0x41800000, v136
	v_mul_f32_e32 v94, 0x41800000, v137
	v_med3_f32 v85, v85, s31, v112
	v_med3_f32 v94, v94, s31, v112
	v_mov_b32_e32 v96, 0
	v_cvt_pk_fp8_f32 v96, v85, v94
	v_mul_f32_e32 v95, 0x41800000, v128
	v_mul_f32_e32 v85, 0x41800000, v129
	v_med3_f32 v94, v95, s31, v112
	v_med3_f32 v85, v85, s31, v112
	v_cvt_pk_fp8_f32 v96, v94, v85 op_sel:[0,0,1]
	v_mov_b32_e32 v94, v92
	v_mov_b32_e32 v95, v90
	v_pk_mul_f32 v[94:95], v[66:67], v[94:95] op_sel_hi:[0,1]
	v_mov_b32_e32 v90, v93
	v_pk_mul_f32 v[90:91], v[66:67], v[90:91] op_sel_hi:[0,1]
	v_pk_fma_f32 v[140:141], v[54:55], v[94:95], v[22:23]
	v_pk_fma_f32 v[138:139], v[56:57], v[90:91], v[24:25]
	v_mul_f32_e32 v85, 0x41800000, v140
	v_mul_f32_e32 v90, 0x41800000, v141
	v_med3_f32 v85, v85, s31, v112
	v_med3_f32 v90, v90, s31, v112
	v_mov_b32_e32 v92, 0
	v_cvt_pk_fp8_f32 v92, v85, v90
	v_mul_f32_e32 v91, 0x41800000, v138
	v_mul_f32_e32 v85, 0x41800000, v139
	v_pk_mul_f32 v[86:87], v[86:87], v[66:67] op_sel_hi:[1,0]
	v_med3_f32 v90, v91, s31, v112
	v_med3_f32 v85, v85, s31, v112
	v_pk_fma_f32 v[144:145], v[58:59], v[86:87], v[26:27]
	v_cvt_pk_fp8_f32 v92, v90, v85 op_sel:[0,0,1]
	v_pk_mul_f32 v[88:89], v[88:89], v[66:67] op_sel_hi:[1,0]
	v_mul_f32_e32 v85, 0x41800000, v144
	v_mul_f32_e32 v86, 0x41800000, v145
	v_pk_fma_f32 v[142:143], v[60:61], v[88:89], v[28:29]
	v_med3_f32 v85, v85, s31, v112
	v_med3_f32 v86, v86, s31, v112
	v_mov_b32_e32 v88, 0
	v_cvt_pk_fp8_f32 v88, v85, v86
	v_mul_f32_e32 v87, 0x41800000, v142
	v_mul_f32_e32 v85, 0x41800000, v143
	v_med3_f32 v86, v87, s31, v112
	v_med3_f32 v85, v85, s31, v112
	v_cvt_pk_fp8_f32 v88, v86, v85 op_sel:[0,0,1]
	v_mov_b32_e32 v85, v146
	v_pk_mul_f32 v[84:85], v[84:85], v[66:67] op_sel_hi:[1,0]
	v_pk_mul_f32 v[82:83], v[82:83], v[66:67] op_sel_hi:[1,0]
	v_mov_b32_e32 v86, 0
	v_pk_fma_f32 v[146:147], v[64:65], v[82:83], v[32:33]
	v_pk_fma_f32 v[82:83], v[62:63], v[84:85], v[30:31]
	v_mul_f32_e32 v85, 0x41800000, v146
	v_mul_f32_e32 v66, 0x41800000, v82
	v_mul_f32_e32 v84, 0x41800000, v83
	v_med3_f32 v66, v66, s31, v112
	v_med3_f32 v84, v84, s31, v112
	v_cvt_pk_fp8_f32 v86, v66, v84
	v_mul_f32_e32 v66, 0x41800000, v147
	v_med3_f32 v84, v85, s31, v112
	v_med3_f32 v66, v66, s31, v112
	v_cvt_pk_fp8_f32 v86, v84, v66 op_sel:[0,0,1]
	global_store_dword v[134:135], v96, off offset:1024
	global_store_dword v[134:135], v92, off offset:1280
	global_store_dword v[134:135], v88, off offset:1536
	global_store_dword v[134:135], v86, off offset:1792
	v_cvt_pk_bf16_f32 v166, v130, v131
	v_cvt_pk_bf16_f32 v167, v132, v133
	v_cvt_pk_bf16_f32 v168, v118, v119
	v_cvt_pk_bf16_f32 v169, v116, v117
	v_cvt_pk_bf16_f32 v170, v122, v123
	v_cvt_pk_bf16_f32 v171, v120, v121
	v_cvt_pk_bf16_f32 v172, v126, v127
	v_cvt_pk_bf16_f32 v173, v124, v125
	v_cvt_pk_bf16_f32 v174, v136, v137
	v_cvt_pk_bf16_f32 v175, v128, v129
	v_cvt_pk_bf16_f32 v176, v140, v141
	v_cvt_pk_bf16_f32 v177, v138, v139
	v_cvt_pk_bf16_f32 v178, v144, v145
	v_cvt_pk_bf16_f32 v179, v142, v143
	v_cvt_pk_bf16_f32 v180, v82, v83
	v_cvt_pk_bf16_f32 v181, v146, v147
	ds_read2st64_b64 v[116:119], v103 offset1:1
	ds_read2st64_b64 v[120:123], v103 offset0:8 offset1:9
	ds_read2st64_b64 v[124:127], v103 offset0:16 offset1:17
	ds_read2st64_b64 v[128:131], v103 offset0:24 offset1:25
	v_mov_b32_e32 v83, 0
	ds_read2st64_b64 v[132:135], v103 offset0:2 offset1:3
	ds_read2st64_b64 v[136:139], v103 offset0:10 offset1:11
	s_waitcnt lgkmcnt(5)
; #define LAS __attribute__((address_space(3)))
; __device__ __forceinline__ void phase_norm2(Frame& F, int l) {
;     ...
;         for (int eg = 0; eg < NE; eg += 4) { float s0 = 0.f, s1 = 0.f, s2 = 0.f, s3 = 0.f;
; #pragma unroll
;             for (int j = 0; j < 8; ++j) { const int o = j * 256 + 4 * F.lane;
;                 const v2u w0 = *(const LAS v2u*)(rwt + eg * DM + o), w1 = *(const LAS v2u*)(rwt + (eg + 1) * DM + o), w2 = *(const LAS v2u*)(rwt + (eg + 2) * DM + o), w3 = *(const LAS v2u*)(rwt + (eg + 3) * DM + o);
;                 const unsigned w0x = w0.x, w0y = w0.y, w1x = w1.x, w1y = w1.y, w2x = w2.x, w2y = w2.y, w3x = w3.x, w3y = w3.y, xlo = xb[j][0], xhi = xb[j][1];
;                 const bf2_t xl = __builtin_bit_cast(bf2_t, xlo), xh = __builtin_bit_cast(bf2_t, xhi);
;                 s0 = __builtin_amdgcn_fdot2_f32_bf16(xl, __builtin_bit_cast(bf2_t, w0x), s0, false); s0 = __builtin_amdgcn_fdot2_f32_bf16(xh, __builtin_bit_cast(bf2_t, w0y), s0, false);
;                 s1 = __builtin_amdgcn_fdot2_f32_bf16(xl, __builtin_bit_cast(bf2_t, w1x), s1, false); s1 = __builtin_amdgcn_fdot2_f32_bf16(xh, __builtin_bit_cast(bf2_t, w1y), s1, false);
;                 s2 = __builtin_amdgcn_fdot2_f32_bf16(xl, __builtin_bit_cast(bf2_t, w2x), s2, false); s2 = __builtin_amdgcn_fdot2_f32_bf16(xh, __builtin_bit_cast(bf2_t, w2y), s2, false);
;                 s3 = __builtin_amdgcn_fdot2_f32_bf16(xl, __builtin_bit_cast(bf2_t, w3x), s3, false); s3 = __builtin_amdgcn_fdot2_f32_bf16(xh, __builtin_bit_cast(bf2_t, w3y), s3, false); }
;             p[eg] = s0; p[eg + 1] = s1; p[eg + 2] = s2; p[eg + 3] = s3; __builtin_amdgcn_sched_barrier(0); }
	v_mfma_f32_4x4x4_16b_bf16 v[182:185], v[116:117], v[166:167], 0
	v_mov_b32_e32 v88, 0
	v_mov_b32_e32 v91, 0
	ds_read2st64_b64 v[140:143], v103 offset0:18 offset1:19
	ds_read2st64_b64 v[144:147], v103 offset0:26 offset1:27
	v_mov_b32_e32 v92, 0
	v_mfma_f32_4x4x4_16b_bf16 v[182:185], v[118:119], v[168:169], v[182:185]
	s_waitcnt lgkmcnt(6)
	v_mfma_f32_4x4x4_16b_bf16 v[186:189], v[120:121], v[166:167], 0
	s_waitcnt lgkmcnt(5)
	v_mfma_f32_4x4x4_16b_bf16 v[190:193], v[124:125], v[166:167], 0
	s_waitcnt lgkmcnt(4)
	v_mfma_f32_4x4x4_16b_bf16 v[194:197], v[128:129], v[166:167], 0
	s_waitcnt lgkmcnt(3)
	v_mfma_f32_4x4x4_16b_bf16 v[182:185], v[132:133], v[170:171], v[182:185]
	v_mfma_f32_4x4x4_16b_bf16 v[186:189], v[122:123], v[168:169], v[186:189]
	v_mfma_f32_4x4x4_16b_bf16 v[190:193], v[126:127], v[168:169], v[190:193]
	v_mfma_f32_4x4x4_16b_bf16 v[194:197], v[130:131], v[168:169], v[194:197]
	v_mfma_f32_4x4x4_16b_bf16 v[182:185], v[134:135], v[172:173], v[182:185]
	s_waitcnt lgkmcnt(2)
	v_mfma_f32_4x4x4_16b_bf16 v[186:189], v[136:137], v[170:171], v[186:189]
	s_waitcnt lgkmcnt(1)
	v_mfma_f32_4x4x4_16b_bf16 v[190:193], v[140:141], v[170:171], v[190:193]
	s_waitcnt lgkmcnt(0)
	v_mfma_f32_4x4x4_16b_bf16 v[194:197], v[144:145], v[170:171], v[194:197]
	ds_read2st64_b64 v[116:119], v103 offset0:4 offset1:5
	ds_read2st64_b64 v[120:123], v103 offset0:12 offset1:13
	ds_read2st64_b64 v[124:127], v103 offset0:20 offset1:21
	ds_read2st64_b64 v[128:131], v103 offset0:28 offset1:29
	ds_read2st64_b64 v[132:135], v103 offset0:6 offset1:7
	v_mfma_f32_4x4x4_16b_bf16 v[186:189], v[138:139], v[172:173], v[186:189]
	v_mfma_f32_4x4x4_16b_bf16 v[190:193], v[142:143], v[172:173], v[190:193]
	v_mfma_f32_4x4x4_16b_bf16 v[194:197], v[146:147], v[172:173], v[194:197]
	s_waitcnt lgkmcnt(4)
	v_mfma_f32_4x4x4_16b_bf16 v[182:185], v[116:117], v[174:175], v[182:185]
	ds_read2st64_b64 v[136:139], v103 offset0:14 offset1:15
	ds_read2st64_b64 v[140:143], v103 offset0:22 offset1:23
	ds_read2st64_b64 v[144:147], v103 offset0:30 offset1:31
	s_waitcnt lgkmcnt(6)
	v_mfma_f32_4x4x4_16b_bf16 v[186:189], v[120:121], v[174:175], v[186:189]
	s_waitcnt lgkmcnt(5)
	v_mfma_f32_4x4x4_16b_bf16 v[190:193], v[124:125], v[174:175], v[190:193]
	s_waitcnt lgkmcnt(4)
	v_mfma_f32_4x4x4_16b_bf16 v[194:197], v[128:129], v[174:175], v[194:197]
	v_mfma_f32_4x4x4_16b_bf16 v[182:185], v[118:119], v[176:177], v[182:185]
	v_mfma_f32_4x4x4_16b_bf16 v[186:189], v[122:123], v[176:177], v[186:189]
	v_mfma_f32_4x4x4_16b_bf16 v[190:193], v[126:127], v[176:177], v[190:193]
	v_mfma_f32_4x4x4_16b_bf16 v[194:197], v[130:131], v[176:177], v[194:197]
	s_waitcnt lgkmcnt(3)
	v_mfma_f32_4x4x4_16b_bf16 v[182:185], v[132:133], v[178:179], v[182:185]
	s_waitcnt lgkmcnt(2)
	v_mfma_f32_4x4x4_16b_bf16 v[186:189], v[136:137], v[178:179], v[186:189]
	s_waitcnt lgkmcnt(1)
	v_mfma_f32_4x4x4_16b_bf16 v[190:193], v[140:141], v[178:179], v[190:193]
	s_waitcnt lgkmcnt(0)
	v_mfma_f32_4x4x4_16b_bf16 v[194:197], v[144:145], v[178:179], v[194:197]
	v_mfma_f32_4x4x4_16b_bf16 v[182:185], v[134:135], v[180:181], v[182:185]
	v_mfma_f32_4x4x4_16b_bf16 v[186:189], v[138:139], v[180:181], v[186:189]
	v_mfma_f32_4x4x4_16b_bf16 v[190:193], v[142:143], v[180:181], v[190:193]
	v_mfma_f32_4x4x4_16b_bf16 v[194:197], v[146:147], v[180:181], v[194:197]
	s_mov_b32 s98, 0x22222222
	s_mov_b32 s99, 0x22222222
	s_mov_b32 s100, 0x44444444
	s_mov_b32 s101, 0x44444444
	s_mov_b32 vcc_lo, 0x88888888
	s_mov_b32 vcc_hi, 0x88888888
	s_nop 4
	v_cndmask_b32_e64 v83, v182, v183, s[98:99]
	v_cndmask_b32_e64 v83, v83, v184, s[100:101]
	v_cndmask_b32_e32 v83, v83, v185, vcc
	v_cndmask_b32_e64 v88, v186, v187, s[98:99]
	v_cndmask_b32_e64 v88, v88, v188, s[100:101]
	v_cndmask_b32_e32 v88, v88, v189, vcc
	v_cndmask_b32_e64 v91, v190, v191, s[98:99]
	v_cndmask_b32_e64 v91, v91, v192, s[100:101]
	v_cndmask_b32_e32 v91, v91, v193, vcc
	v_cndmask_b32_e64 v92, v194, v195, s[98:99]
	v_cndmask_b32_e64 v92, v92, v196, s[100:101]
	v_cndmask_b32_e32 v92, v92, v197, vcc
	ds_read2st64_b64 v[118:121], v103 offset0:32 offset1:33
	ds_read2st64_b64 v[122:125], v103 offset0:40 offset1:41
	ds_read2st64_b64 v[126:129], v103 offset0:48 offset1:49
	ds_read2st64_b64 v[130:133], v103 offset0:56 offset1:57
	v_mov_b32_e32 v116, 0
	ds_read2st64_b64 v[134:137], v103 offset0:34 offset1:35
	ds_read2st64_b64 v[138:141], v103 offset0:42 offset1:43
	s_waitcnt lgkmcnt(5)
	v_mfma_f32_4x4x4_16b_bf16 v[218:221], v[118:119], v[166:167], 0
	v_mov_b32_e32 v118, 0
	s_waitcnt lgkmcnt(4)
	v_mfma_f32_4x4x4_16b_bf16 v[222:225], v[122:123], v[166:167], 0
	v_mov_b32_e32 v119, 0
	ds_read2st64_b64 v[142:145], v103 offset0:50 offset1:51
	ds_read2st64_b64 v[146:149], v103 offset0:58 offset1:59
	v_mov_b32_e32 v117, 0
	v_mfma_f32_4x4x4_16b_bf16 v[218:221], v[120:121], v[168:169], v[218:221]
	s_waitcnt lgkmcnt(5)
	v_mfma_f32_4x4x4_16b_bf16 v[226:229], v[126:127], v[166:167], 0
	s_waitcnt lgkmcnt(4)
	v_mfma_f32_4x4x4_16b_bf16 v[230:233], v[130:131], v[166:167], 0
	v_mfma_f32_4x4x4_16b_bf16 v[222:225], v[124:125], v[168:169], v[222:225]
	s_waitcnt lgkmcnt(3)
	v_mfma_f32_4x4x4_16b_bf16 v[218:221], v[134:135], v[170:171], v[218:221]
	v_mfma_f32_4x4x4_16b_bf16 v[226:229], v[128:129], v[168:169], v[226:229]
	v_mfma_f32_4x4x4_16b_bf16 v[230:233], v[132:133], v[168:169], v[230:233]
	s_waitcnt lgkmcnt(2)
	v_mfma_f32_4x4x4_16b_bf16 v[222:225], v[138:139], v[170:171], v[222:225]
	v_mfma_f32_4x4x4_16b_bf16 v[218:221], v[136:137], v[172:173], v[218:221]
	s_waitcnt lgkmcnt(1)
	v_mfma_f32_4x4x4_16b_bf16 v[226:229], v[142:143], v[170:171], v[226:229]
	s_waitcnt lgkmcnt(0)
; #define LAS __attribute__((address_space(3)))
; __device__ __forceinline__ void phase_norm2(Frame& F, int l) {
;     ...
;         for (int eg = 0; eg < NE; eg += 4) { float s0 = 0.f, s1 = 0.f, s2 = 0.f, s3 = 0.f;
; #pragma unroll
;             for (int j = 0; j < 8; ++j) { const int o = j * 256 + 4 * F.lane;
;                 const v2u w0 = *(const LAS v2u*)(rwt + eg * DM + o), w1 = *(const LAS v2u*)(rwt + (eg + 1) * DM + o), w2 = *(const LAS v2u*)(rwt + (eg + 2) * DM + o), w3 = *(const LAS v2u*)(rwt + (eg + 3) * DM + o);
;                 const unsigned w0x = w0.x, w0y = w0.y, w1x = w1.x, w1y = w1.y, w2x = w2.x, w2y = w2.y, w3x = w3.x, w3y = w3.y, xlo = xb[j][0], xhi = xb[j][1];
;                 const bf2_t xl = __builtin_bit_cast(bf2_t, xlo), xh = __builtin_bit_cast(bf2_t, xhi);
;                 s0 = __builtin_amdgcn_fdot2_f32_bf16(xl, __builtin_bit_cast(bf2_t, w0x), s0, false); s0 = __builtin_amdgcn_fdot2_f32_bf16(xh, __builtin_bit_cast(bf2_t, w0y), s0, false);
;                 s1 = __builtin_amdgcn_fdot2_f32_bf16(xl, __builtin_bit_cast(bf2_t, w1x), s1, false); s1 = __builtin_amdgcn_fdot2_f32_bf16(xh, __builtin_bit_cast(bf2_t, w1y), s1, false);
;                 s2 = __builtin_amdgcn_fdot2_f32_bf16(xl, __builtin_bit_cast(bf2_t, w2x), s2, false); s2 = __builtin_amdgcn_fdot2_f32_bf16(xh, __builtin_bit_cast(bf2_t, w2y), s2, false);
;                 s3 = __builtin_amdgcn_fdot2_f32_bf16(xl, __builtin_bit_cast(bf2_t, w3x), s3, false); s3 = __builtin_amdgcn_fdot2_f32_bf16(xh, __builtin_bit_cast(bf2_t, w3y), s3, false); }
;             p[eg] = s0; p[eg + 1] = s1; p[eg + 2] = s2; p[eg + 3] = s3; __builtin_amdgcn_sched_barrier(0); }
	v_mfma_f32_4x4x4_16b_bf16 v[230:233], v[146:147], v[170:171], v[230:233]
	ds_read2st64_b64 v[120:123], v103 offset0:36 offset1:37
	ds_read2st64_b64 v[124:127], v103 offset0:44 offset1:45
	ds_read2st64_b64 v[128:131], v103 offset0:52 offset1:53
	ds_read2st64_b64 v[132:135], v103 offset0:60 offset1:61
	ds_read2st64_b64 v[136:139], v103 offset0:38 offset1:39
	v_mfma_f32_4x4x4_16b_bf16 v[222:225], v[140:141], v[172:173], v[222:225]
	v_mfma_f32_4x4x4_16b_bf16 v[226:229], v[144:145], v[172:173], v[226:229]
	v_mfma_f32_4x4x4_16b_bf16 v[230:233], v[148:149], v[172:173], v[230:233]
	ds_read2st64_b64 v[140:143], v103 offset0:46 offset1:47
	ds_read2st64_b64 v[144:147], v103 offset0:54 offset1:55
	ds_read2st64_b64 v[148:151], v103 offset0:62 offset1:63
	s_waitcnt lgkmcnt(7)
	v_mfma_f32_4x4x4_16b_bf16 v[218:221], v[120:121], v[174:175], v[218:221]
	s_waitcnt lgkmcnt(6)
	v_mfma_f32_4x4x4_16b_bf16 v[222:225], v[124:125], v[174:175], v[222:225]
	s_waitcnt lgkmcnt(5)
	v_mfma_f32_4x4x4_16b_bf16 v[226:229], v[128:129], v[174:175], v[226:229]
	s_waitcnt lgkmcnt(4)
	v_mfma_f32_4x4x4_16b_bf16 v[230:233], v[132:133], v[174:175], v[230:233]
	v_mfma_f32_4x4x4_16b_bf16 v[218:221], v[122:123], v[176:177], v[218:221]
	v_mfma_f32_4x4x4_16b_bf16 v[222:225], v[126:127], v[176:177], v[222:225]
	v_mfma_f32_4x4x4_16b_bf16 v[226:229], v[130:131], v[176:177], v[226:229]
	v_mfma_f32_4x4x4_16b_bf16 v[230:233], v[134:135], v[176:177], v[230:233]
	s_waitcnt lgkmcnt(3)
	v_mfma_f32_4x4x4_16b_bf16 v[218:221], v[136:137], v[178:179], v[218:221]
	s_waitcnt lgkmcnt(2)
	v_mfma_f32_4x4x4_16b_bf16 v[222:225], v[140:141], v[178:179], v[222:225]
	s_waitcnt lgkmcnt(1)
	v_mfma_f32_4x4x4_16b_bf16 v[226:229], v[144:145], v[178:179], v[226:229]
	s_waitcnt lgkmcnt(0)
	v_mfma_f32_4x4x4_16b_bf16 v[230:233], v[148:149], v[178:179], v[230:233]
	v_mfma_f32_4x4x4_16b_bf16 v[218:221], v[138:139], v[180:181], v[218:221]
	v_mfma_f32_4x4x4_16b_bf16 v[222:225], v[142:143], v[180:181], v[222:225]
	v_mfma_f32_4x4x4_16b_bf16 v[226:229], v[146:147], v[180:181], v[226:229]
	v_mfma_f32_4x4x4_16b_bf16 v[230:233], v[150:151], v[180:181], v[230:233]
	s_mov_b32 s98, 0x22222222
	s_mov_b32 s99, 0x22222222
	s_mov_b32 s100, 0x44444444
	s_mov_b32 s101, 0x44444444
	s_mov_b32 vcc_lo, 0x88888888
	s_mov_b32 vcc_hi, 0x88888888
	s_nop 4
	v_cndmask_b32_e64 v116, v218, v219, s[98:99]
	v_cndmask_b32_e64 v116, v116, v220, s[100:101]
	v_cndmask_b32_e32 v116, v116, v221, vcc
	v_cndmask_b32_e64 v118, v222, v223, s[98:99]
	v_cndmask_b32_e64 v118, v118, v224, s[100:101]
	v_cndmask_b32_e32 v118, v118, v225, vcc
	v_cndmask_b32_e64 v119, v226, v227, s[98:99]
	v_cndmask_b32_e64 v119, v119, v228, s[100:101]
	v_cndmask_b32_e32 v119, v119, v229, vcc
	v_cndmask_b32_e64 v117, v230, v231, s[98:99]
	v_cndmask_b32_e64 v117, v117, v232, s[100:101]
	v_cndmask_b32_e32 v117, v117, v233, vcc
	ds_read2st64_b64 v[120:123], v103 offset0:64 offset1:65
	ds_read2st64_b64 v[124:127], v103 offset0:72 offset1:73
	ds_read2st64_b64 v[128:131], v103 offset0:80 offset1:81
	ds_read2st64_b64 v[132:135], v103 offset0:88 offset1:89
	v_mov_b32_e32 v152, 0
	ds_read2st64_b64 v[136:139], v103 offset0:66 offset1:67
	ds_read2st64_b64 v[140:143], v103 offset0:74 offset1:75
	s_waitcnt lgkmcnt(5)
	v_mfma_f32_4x4x4_16b_bf16 v[182:185], v[120:121], v[166:167], 0
	v_mov_b32_e32 v153, 0
	v_mov_b32_e32 v154, 0
	ds_read2st64_b64 v[144:147], v103 offset0:82 offset1:83
	ds_read2st64_b64 v[148:151], v103 offset0:90 offset1:91
	v_mov_b32_e32 v155, 0
	v_mfma_f32_4x4x4_16b_bf16 v[182:185], v[122:123], v[168:169], v[182:185]
	s_waitcnt lgkmcnt(6)
	v_mfma_f32_4x4x4_16b_bf16 v[186:189], v[124:125], v[166:167], 0
	s_waitcnt lgkmcnt(5)
	v_mfma_f32_4x4x4_16b_bf16 v[190:193], v[128:129], v[166:167], 0
	s_waitcnt lgkmcnt(4)
	v_mfma_f32_4x4x4_16b_bf16 v[194:197], v[132:133], v[166:167], 0
	s_waitcnt lgkmcnt(3)
	v_mfma_f32_4x4x4_16b_bf16 v[182:185], v[136:137], v[170:171], v[182:185]
	v_mfma_f32_4x4x4_16b_bf16 v[186:189], v[126:127], v[168:169], v[186:189]
	v_mfma_f32_4x4x4_16b_bf16 v[190:193], v[130:131], v[168:169], v[190:193]
	v_mfma_f32_4x4x4_16b_bf16 v[194:197], v[134:135], v[168:169], v[194:197]
	v_mfma_f32_4x4x4_16b_bf16 v[182:185], v[138:139], v[172:173], v[182:185]
	s_waitcnt lgkmcnt(2)
	v_mfma_f32_4x4x4_16b_bf16 v[186:189], v[140:141], v[170:171], v[186:189]
	s_waitcnt lgkmcnt(1)
	v_mfma_f32_4x4x4_16b_bf16 v[190:193], v[144:145], v[170:171], v[190:193]
	s_waitcnt lgkmcnt(0)
	v_mfma_f32_4x4x4_16b_bf16 v[194:197], v[148:149], v[170:171], v[194:197]
	ds_read2st64_b64 v[120:123], v103 offset0:68 offset1:69
	ds_read2st64_b64 v[124:127], v103 offset0:76 offset1:77
	ds_read2st64_b64 v[128:131], v103 offset0:84 offset1:85
	ds_read2st64_b64 v[132:135], v103 offset0:92 offset1:93
	ds_read2st64_b64 v[136:139], v103 offset0:70 offset1:71
	v_mfma_f32_4x4x4_16b_bf16 v[186:189], v[142:143], v[172:173], v[186:189]
	v_mfma_f32_4x4x4_16b_bf16 v[190:193], v[146:147], v[172:173], v[190:193]
	v_mfma_f32_4x4x4_16b_bf16 v[194:197], v[150:151], v[172:173], v[194:197]
	ds_read2st64_b64 v[140:143], v103 offset0:78 offset1:79
	ds_read2st64_b64 v[144:147], v103 offset0:86 offset1:87
	ds_read2st64_b64 v[148:151], v103 offset0:94 offset1:95
	s_waitcnt lgkmcnt(7)
	v_mfma_f32_4x4x4_16b_bf16 v[182:185], v[120:121], v[174:175], v[182:185]
	s_waitcnt lgkmcnt(6)
	v_mfma_f32_4x4x4_16b_bf16 v[186:189], v[124:125], v[174:175], v[186:189]
	s_waitcnt lgkmcnt(5)
	v_mfma_f32_4x4x4_16b_bf16 v[190:193], v[128:129], v[174:175], v[190:193]
	s_waitcnt lgkmcnt(4)
; #define LAS __attribute__((address_space(3)))
; __device__ __forceinline__ void phase_norm2(Frame& F, int l) {
;     ...
;         for (int eg = 0; eg < NE; eg += 4) { float s0 = 0.f, s1 = 0.f, s2 = 0.f, s3 = 0.f;
; #pragma unroll
;             for (int j = 0; j < 8; ++j) { const int o = j * 256 + 4 * F.lane;
;                 const v2u w0 = *(const LAS v2u*)(rwt + eg * DM + o), w1 = *(const LAS v2u*)(rwt + (eg + 1) * DM + o), w2 = *(const LAS v2u*)(rwt + (eg + 2) * DM + o), w3 = *(const LAS v2u*)(rwt + (eg + 3) * DM + o);
;                 const unsigned w0x = w0.x, w0y = w0.y, w1x = w1.x, w1y = w1.y, w2x = w2.x, w2y = w2.y, w3x = w3.x, w3y = w3.y, xlo = xb[j][0], xhi = xb[j][1];
;                 const bf2_t xl = __builtin_bit_cast(bf2_t, xlo), xh = __builtin_bit_cast(bf2_t, xhi);
;                 s0 = __builtin_amdgcn_fdot2_f32_bf16(xl, __builtin_bit_cast(bf2_t, w0x), s0, false); s0 = __builtin_amdgcn_fdot2_f32_bf16(xh, __builtin_bit_cast(bf2_t, w0y), s0, false);
;                 s1 = __builtin_amdgcn_fdot2_f32_bf16(xl, __builtin_bit_cast(bf2_t, w1x), s1, false); s1 = __builtin_amdgcn_fdot2_f32_bf16(xh, __builtin_bit_cast(bf2_t, w1y), s1, false);
;                 s2 = __builtin_amdgcn_fdot2_f32_bf16(xl, __builtin_bit_cast(bf2_t, w2x), s2, false); s2 = __builtin_amdgcn_fdot2_f32_bf16(xh, __builtin_bit_cast(bf2_t, w2y), s2, false);
;                 s3 = __builtin_amdgcn_fdot2_f32_bf16(xl, __builtin_bit_cast(bf2_t, w3x), s3, false); s3 = __builtin_amdgcn_fdot2_f32_bf16(xh, __builtin_bit_cast(bf2_t, w3y), s3, false); }
;             p[eg] = s0; p[eg + 1] = s1; p[eg + 2] = s2; p[eg + 3] = s3; __builtin_amdgcn_sched_barrier(0); }
	v_mfma_f32_4x4x4_16b_bf16 v[194:197], v[132:133], v[174:175], v[194:197]
	v_mfma_f32_4x4x4_16b_bf16 v[182:185], v[122:123], v[176:177], v[182:185]
	v_mfma_f32_4x4x4_16b_bf16 v[186:189], v[126:127], v[176:177], v[186:189]
	v_mfma_f32_4x4x4_16b_bf16 v[190:193], v[130:131], v[176:177], v[190:193]
	v_mfma_f32_4x4x4_16b_bf16 v[194:197], v[134:135], v[176:177], v[194:197]
	s_waitcnt lgkmcnt(3)
	v_mfma_f32_4x4x4_16b_bf16 v[182:185], v[136:137], v[178:179], v[182:185]
	s_waitcnt lgkmcnt(2)
	v_mfma_f32_4x4x4_16b_bf16 v[186:189], v[140:141], v[178:179], v[186:189]
	s_waitcnt lgkmcnt(1)
	v_mfma_f32_4x4x4_16b_bf16 v[190:193], v[144:145], v[178:179], v[190:193]
	s_waitcnt lgkmcnt(0)
	v_mfma_f32_4x4x4_16b_bf16 v[194:197], v[148:149], v[178:179], v[194:197]
	v_mfma_f32_4x4x4_16b_bf16 v[182:185], v[138:139], v[180:181], v[182:185]
	v_mfma_f32_4x4x4_16b_bf16 v[186:189], v[142:143], v[180:181], v[186:189]
	v_mfma_f32_4x4x4_16b_bf16 v[190:193], v[146:147], v[180:181], v[190:193]
	v_mfma_f32_4x4x4_16b_bf16 v[194:197], v[150:151], v[180:181], v[194:197]
	s_mov_b32 s98, 0x22222222
	s_mov_b32 s99, 0x22222222
	s_mov_b32 s100, 0x44444444
	s_mov_b32 s101, 0x44444444
	s_mov_b32 vcc_lo, 0x88888888
	s_mov_b32 vcc_hi, 0x88888888
	s_nop 4
	v_cndmask_b32_e64 v152, v182, v183, s[98:99]
	v_cndmask_b32_e64 v152, v152, v184, s[100:101]
	v_cndmask_b32_e32 v152, v152, v185, vcc
	v_cndmask_b32_e64 v153, v186, v187, s[98:99]
	v_cndmask_b32_e64 v153, v153, v188, s[100:101]
	v_cndmask_b32_e32 v153, v153, v189, vcc
	v_cndmask_b32_e64 v154, v190, v191, s[98:99]
	v_cndmask_b32_e64 v154, v154, v192, s[100:101]
	v_cndmask_b32_e32 v154, v154, v193, vcc
	v_cndmask_b32_e64 v155, v194, v195, s[98:99]
	v_cndmask_b32_e64 v155, v155, v196, s[100:101]
	v_cndmask_b32_e32 v155, v155, v197, vcc
	ds_read2st64_b64 v[120:123], v103 offset0:96 offset1:97
	ds_read2st64_b64 v[124:127], v103 offset0:104 offset1:105
	ds_read2st64_b64 v[128:131], v103 offset0:112 offset1:113
	ds_read2st64_b64 v[132:135], v103 offset0:120 offset1:121
	v_mov_b32_e32 v156, 0
	ds_read2st64_b64 v[136:139], v103 offset0:98 offset1:99
	ds_read2st64_b64 v[140:143], v103 offset0:106 offset1:107
	v_mov_b32_e32 v157, 0
	v_mov_b32_e32 v158, 0
	ds_read2st64_b64 v[144:147], v103 offset0:114 offset1:115
	ds_read2st64_b64 v[148:151], v103 offset0:122 offset1:123
	v_mov_b32_e32 v159, 0
	s_waitcnt lgkmcnt(7)
	v_mfma_f32_4x4x4_16b_bf16 v[218:221], v[120:121], v[166:167], 0
	s_waitcnt lgkmcnt(6)
	v_mfma_f32_4x4x4_16b_bf16 v[222:225], v[124:125], v[166:167], 0
	s_waitcnt lgkmcnt(5)
	v_mfma_f32_4x4x4_16b_bf16 v[226:229], v[128:129], v[166:167], 0
	s_waitcnt lgkmcnt(4)
	v_mfma_f32_4x4x4_16b_bf16 v[230:233], v[132:133], v[166:167], 0
	v_mfma_f32_4x4x4_16b_bf16 v[218:221], v[122:123], v[168:169], v[218:221]
	v_mfma_f32_4x4x4_16b_bf16 v[222:225], v[126:127], v[168:169], v[222:225]
	v_mfma_f32_4x4x4_16b_bf16 v[226:229], v[130:131], v[168:169], v[226:229]
	v_mfma_f32_4x4x4_16b_bf16 v[230:233], v[134:135], v[168:169], v[230:233]
	s_waitcnt lgkmcnt(3)
	v_mfma_f32_4x4x4_16b_bf16 v[218:221], v[136:137], v[170:171], v[218:221]
	s_waitcnt lgkmcnt(2)
	v_mfma_f32_4x4x4_16b_bf16 v[222:225], v[140:141], v[170:171], v[222:225]
	s_waitcnt lgkmcnt(1)
	v_mfma_f32_4x4x4_16b_bf16 v[226:229], v[144:145], v[170:171], v[226:229]
	s_waitcnt lgkmcnt(0)
	v_mfma_f32_4x4x4_16b_bf16 v[230:233], v[148:149], v[170:171], v[230:233]
	v_mfma_f32_4x4x4_16b_bf16 v[218:221], v[138:139], v[172:173], v[218:221]
	v_mfma_f32_4x4x4_16b_bf16 v[222:225], v[142:143], v[172:173], v[222:225]
	v_mfma_f32_4x4x4_16b_bf16 v[226:229], v[146:147], v[172:173], v[226:229]
	v_mfma_f32_4x4x4_16b_bf16 v[230:233], v[150:151], v[172:173], v[230:233]
	ds_read2st64_b64 v[94:97], v103 offset0:100 offset1:101
	ds_read2st64_b64 v[120:123], v103 offset0:108 offset1:109
	ds_read2st64_b64 v[124:127], v103 offset0:116 offset1:117
	ds_read2st64_b64 v[128:131], v103 offset0:124 offset1:125
	ds_read2st64_b64 v[132:135], v103 offset0:102 offset1:103
	ds_read2st64_b64 v[136:139], v103 offset0:110 offset1:111
	ds_read2st64_b64 v[140:143], v103 offset0:118 offset1:119
	ds_read2st64_b64 v[144:147], v103 offset0:126 offset1:127
	s_waitcnt lgkmcnt(7)
	v_mfma_f32_4x4x4_16b_bf16 v[218:221], v[94:95], v[174:175], v[218:221]
	s_waitcnt lgkmcnt(6)
	v_mfma_f32_4x4x4_16b_bf16 v[222:225], v[120:121], v[174:175], v[222:225]
	s_waitcnt lgkmcnt(5)
	v_mfma_f32_4x4x4_16b_bf16 v[226:229], v[124:125], v[174:175], v[226:229]
	s_waitcnt lgkmcnt(4)
	v_mfma_f32_4x4x4_16b_bf16 v[230:233], v[128:129], v[174:175], v[230:233]
	v_mfma_f32_4x4x4_16b_bf16 v[218:221], v[96:97], v[176:177], v[218:221]
	v_mfma_f32_4x4x4_16b_bf16 v[222:225], v[122:123], v[176:177], v[222:225]
	v_mfma_f32_4x4x4_16b_bf16 v[226:229], v[126:127], v[176:177], v[226:229]
	v_mfma_f32_4x4x4_16b_bf16 v[230:233], v[130:131], v[176:177], v[230:233]
	s_waitcnt lgkmcnt(3)
; __device__ __forceinline__ void phase_norm2(Frame& F, int l) {
;     ...
;         for (int eg = 0; eg < NE; eg += 4) { float s0 = 0.f, s1 = 0.f, s2 = 0.f, s3 = 0.f;
; #pragma unroll
;             for (int j = 0; j < 8; ++j) { const int o = j * 256 + 4 * F.lane;
;                 const v2u w0 = *(const LAS v2u*)(rwt + eg * DM + o), w1 = *(const LAS v2u*)(rwt + (eg + 1) * DM + o), w2 = *(const LAS v2u*)(rwt + (eg + 2) * DM + o), w3 = *(const LAS v2u*)(rwt + (eg + 3) * DM + o);
;                 const unsigned w0x = w0.x, w0y = w0.y, w1x = w1.x, w1y = w1.y, w2x = w2.x, w2y = w2.y, w3x = w3.x, w3y = w3.y, xlo = xb[j][0], xhi = xb[j][1];
;                 const bf2_t xl = __builtin_bit_cast(bf2_t, xlo), xh = __builtin_bit_cast(bf2_t, xhi);
;                 s0 = __builtin_amdgcn_fdot2_f32_bf16(xl, __builtin_bit_cast(bf2_t, w0x), s0, false); s0 = __builtin_amdgcn_fdot2_f32_bf16(xh, __builtin_bit_cast(bf2_t, w0y), s0, false);
;                 s1 = __builtin_amdgcn_fdot2_f32_bf16(xl, __builtin_bit_cast(bf2_t, w1x), s1, false); s1 = __builtin_amdgcn_fdot2_f32_bf16(xh, __builtin_bit_cast(bf2_t, w1y), s1, false);
;                 s2 = __builtin_amdgcn_fdot2_f32_bf16(xl, __builtin_bit_cast(bf2_t, w2x), s2, false); s2 = __builtin_amdgcn_fdot2_f32_bf16(xh, __builtin_bit_cast(bf2_t, w2y), s2, false);
;                 s3 = __builtin_amdgcn_fdot2_f32_bf16(xl, __builtin_bit_cast(bf2_t, w3x), s3, false); s3 = __builtin_amdgcn_fdot2_f32_bf16(xh, __builtin_bit_cast(bf2_t, w3y), s3, false); }
;             p[eg] = s0; p[eg + 1] = s1; p[eg + 2] = s2; p[eg + 3] = s3; __builtin_amdgcn_sched_barrier(0); }
;         const bool b5 = (F.lane & 32) != 0, b4 = (F.lane & 16) != 0, b3 = (F.lane & 8) != 0, b2 = (F.lane & 4) != 0;
;         float q8[8], q4[4], q2[2];
; #pragma unroll
;         for (int i = 0; i < 8; ++i) { const float keep = b5 ? p[i + 8] : p[i], give = b5 ? p[i] : p[i + 8]; q8[i] = keep + __shfl_xor(give, 32); }
; #pragma unroll
;         for (int i = 0; i < 4; ++i) { const float keep = b4 ? q8[i + 4] : q8[i], give = b4 ? q8[i] : q8[i + 4]; q4[i] = keep + __shfl_xor(give, 16); }
; #pragma unroll
;         for (int i = 0; i < 2; ++i) { const float keep = b3 ? q4[i + 2] : q4[i], give = b3 ? q4[i] : q4[i + 2]; q2[i] = keep + __shfl_xor(give, 8); }
;         float lg; { const float keep = b2 ? q2[1] : q2[0], give = b2 ? q2[0] : q2[1]; lg = keep + __shfl_xor(give, 4); }
	v_mfma_f32_4x4x4_16b_bf16 v[218:221], v[132:133], v[178:179], v[218:221]
	s_waitcnt lgkmcnt(2)
	v_mfma_f32_4x4x4_16b_bf16 v[222:225], v[136:137], v[178:179], v[222:225]
	s_waitcnt lgkmcnt(1)
	v_mfma_f32_4x4x4_16b_bf16 v[226:229], v[140:141], v[178:179], v[226:229]
	s_waitcnt lgkmcnt(0)
	v_mfma_f32_4x4x4_16b_bf16 v[230:233], v[144:145], v[178:179], v[230:233]
	v_mfma_f32_4x4x4_16b_bf16 v[218:221], v[134:135], v[180:181], v[218:221]
	v_mfma_f32_4x4x4_16b_bf16 v[222:225], v[138:139], v[180:181], v[222:225]
	v_mfma_f32_4x4x4_16b_bf16 v[226:229], v[142:143], v[180:181], v[226:229]
	v_mfma_f32_4x4x4_16b_bf16 v[230:233], v[146:147], v[180:181], v[230:233]
	s_mov_b32 s98, 0x22222222
	s_mov_b32 s99, 0x22222222
	s_mov_b32 s100, 0x44444444
	s_mov_b32 s101, 0x44444444
	s_mov_b32 vcc_lo, 0x88888888
	s_mov_b32 vcc_hi, 0x88888888
	s_nop 4
	v_cndmask_b32_e64 v156, v218, v219, s[98:99]
	v_cndmask_b32_e64 v156, v156, v220, s[100:101]
	v_cndmask_b32_e32 v156, v156, v221, vcc
	v_cndmask_b32_e64 v157, v222, v223, s[98:99]
	v_cndmask_b32_e64 v157, v157, v224, s[100:101]
	v_cndmask_b32_e32 v157, v157, v225, vcc
	v_cndmask_b32_e64 v158, v226, v227, s[98:99]
	v_cndmask_b32_e64 v158, v158, v228, s[100:101]
	v_cndmask_b32_e32 v158, v158, v229, vcc
	v_cndmask_b32_e64 v159, v230, v231, s[98:99]
	v_cndmask_b32_e64 v159, v159, v232, s[100:101]
	v_cndmask_b32_e32 v159, v159, v233, vcc
	s_nop 1
	v_permlane32_swap_b32_e32 v83, v152
	v_permlane32_swap_b32_e32 v88, v153
	v_permlane32_swap_b32_e32 v91, v154
	v_permlane32_swap_b32_e32 v92, v155
	v_permlane32_swap_b32_e32 v116, v156
	v_permlane32_swap_b32_e32 v118, v157
	v_permlane32_swap_b32_e32 v119, v158
	v_permlane32_swap_b32_e32 v117, v159
	v_add_f32_e32 v66, v83, v152
	v_add_f32_e32 v82, v88, v153
	v_add_f32_e32 v83, v91, v154
	v_add_f32_e32 v84, v92, v155
	v_add_f32_e32 v85, v116, v156
	v_add_f32_e32 v86, v118, v157
	v_add_f32_e32 v87, v119, v158
	v_add_f32_e32 v88, v117, v159
	s_nop 1
	v_permlane16_swap_b32_e32 v66, v85
	v_permlane16_swap_b32_e32 v82, v86
	v_permlane16_swap_b32_e32 v83, v87
	v_permlane16_swap_b32_e32 v84, v88
	v_add_f32_e32 v66, v66, v85
	v_add_f32_e32 v82, v82, v86
	v_add_f32_e32 v83, v83, v87
	v_add_f32_e32 v84, v84, v88
	v_cndmask_b32_e64 v85, v66, v83, s[8:9]
	v_cndmask_b32_e64 v86, v82, v84, s[8:9]
	v_cndmask_b32_e64 v66, v83, v66, s[8:9]
	v_cndmask_b32_e64 v82, v84, v82, s[8:9]
	s_nop 0
	v_add_f32_dpp v66, v85, v66 row_ror:8 row_mask:0xf bank_mask:0xf
	v_add_f32_dpp v82, v86, v82 row_ror:8 row_mask:0xf bank_mask:0xf
	v_cndmask_b32_e64 v83, v66, v82, s[10:11]
	v_cndmask_b32_e64 v66, v82, v66, s[10:11]
	s_nop 1
	v_mov_b32_dpp v84, v83 row_half_mirror row_mask:0xf bank_mask:0xf
	s_nop 1
	v_add_f32_dpp v66, v84, v66 quad_perm:[3,2,1,0] row_mask:0xf bank_mask:0xf
	s_nop 1
	v_add_f32_dpp v82, v66, v66 quad_perm:[2,3,0,1] row_mask:0xf bank_mask:0xf
	s_nop 1
	v_add_f32_dpp v66, v82, v82 quad_perm:[1,0,3,2] row_mask:0xf bank_mask:0xf
	s_nop 1
	v_mov_b32_dpp v83, v66 row_half_mirror row_mask:0xf bank_mask:0xf
	s_nop 1
	v_max_f32_dpp v82, v83, v66 quad_perm:[3,2,1,0] row_mask:0xf bank_mask:0xf
	s_nop 1
	v_max_f32_dpp v83, v82, v82 row_ror:8 row_mask:0xf bank_mask:0xf
	v_mov_b32_e32 v82, v83
	s_nop 1
	v_permlane16_swap_b32_e32 v83, v82
	v_max_f32_e32 v82, v83, v82
	v_mov_b32_e32 v83, v82
	s_nop 1
	v_permlane32_swap_b32_e32 v82, v83
	v_max_f32_e32 v82, v82, v83
	v_sub_f32_e32 v66, v66, v82
	v_mul_f32_e32 v66, 0x3fb8aa3b, v66
	v_exp_f32_e32 v66, v66
	s_nop 1
	v_mov_b32_dpp v83, v66 row_half_mirror row_mask:0xf bank_mask:0xf
	s_nop 1
	v_add_f32_dpp v82, v83, v66 quad_perm:[3,2,1,0] row_mask:0xf bank_mask:0xf
	s_nop 1
	v_add_f32_dpp v83, v82, v82 row_ror:8 row_mask:0xf bank_mask:0xf
	v_mov_b32_e32 v82, v83
	s_nop 1
	v_permlane16_swap_b32_e32 v83, v82
	v_add_f32_e32 v82, v83, v82
	v_mov_b32_e32 v83, v82
	s_nop 1
	v_permlane32_swap_b32_e32 v82, v83
	v_add_f32_e32 v82, v82, v83
	s_and_saveexec_b64 s[0:1], s[12:13]
	s_cbranch_execz .LBB0_915
	s_waitcnt lgkmcnt(0)
	s_nop 0
	v_div_scale_f32 v83, s[14:15], v82, v82, v66
	v_rcp_f32_e32 v84, v83
	v_div_scale_f32 v85, vcc, v66, v82, v66
	s_cmpk_gt_i32 s16, 0x3fff
	v_fma_f32 v86, -v83, v84, 1.0
	v_fmac_f32_e32 v84, v86, v84
	v_mul_f32_e32 v86, v85, v84
	v_fma_f32 v87, -v83, v86, v85
	v_fmac_f32_e32 v86, v87, v84
	v_fma_f32 v83, -v83, v86, v85
	v_div_fmas_f32 v83, v83, v84, v86
	v_div_fixup_f32 v82, v83, v82, v66
	s_mov_b64 s[14:15], -1
	s_cbranch_scc0 .LBB0_921
	s_add_i32 s14, s16, 0xffffc000
	s_lshr_b32 s14, s14, 4
	s_and_b32 s14, s14, 0xffffff0
	v_or_b32_e32 v66, s14, v104
	s_and_b32 s14, s16, 0xff
	v_lshlrev_b64 v[84:85], 10, v[66:67]
	v_lshl_add_u64 v[84:85], s[20:21], 0, v[84:85]
	s_lshl_b32 s18, s14, 2
	v_lshl_add_u64 v[84:85], v[84:85], 0, s[18:19]
	global_store_dword v[84:85], v82, off
	s_mov_b64 s[14:15], 0

; #define GAS __attribute__((address_space(1)))
; __device__ __forceinline__ f32x4 ld_bf4(const bf16* p) { const v2u w = *(const GAS v2u*)p; return (f32x4){bflo(w.x), bfhi(w.x), bflo(w.y), bfhi(w.y)}; }
; __device__ __forceinline__ float row_rs(const f32x4 (&x)[8]) {
;     float s = 0.f;
; #pragma unroll
;     for (int j = 0; j < 8; ++j) s += (x[j][0] * x[j][0] + x[j][1] * x[j][1]) + (x[j][2] * x[j][2] + x[j][3] * x[j][3]);
;     return 1.0f / sqrtf(wave_sum(s) * (1.0f / DM) + EPS);
; }
; __device__ __forceinline__ void phase_norm2(Frame& F, int l) {
;     ...
;         const int rb = r < ML ? (r >> 11) : 8; const bf16* xr = WSP(bf16, WS_XM) + (size_t)r * DM;
;         f32x4 x[8];
; #pragma unroll
;         for (int j = 0; j < 8; ++j) x[j] = ld_bf4(xr + j * 256 + 4 * F.lane);
;         if (rb != rb_cur) { rb_cur = rb; const float* sh = modl + (size_t)(rb * 6 + 3) * DM; const float* sc = modl + (size_t)(rb * 6 + 4) * DM;
; #pragma unroll
;             for (int j = 0; j < 8; ++j) { const int c = j * 256 + 4 * F.lane; ga[j] = *(const GAS f32x4*)(gn + c) * (1.0f + *(const GAS f32x4*)(sc + c)); sb[j] = *(const GAS f32x4*)(sh + c); } }
;         const float rs = row_rs(x);
;         unsigned char* ho = WSP(unsigned char, WS_H) + (size_t)r * DM;
; #pragma unroll
;         for (int j = 0; j < 8; ++j) { const int c = j * 256 + 4 * F.lane;
;             x[j] = x[j] * rs * ga[j] + sb[j]; *(GAS unsigned*)(ho + c) = pk4_fp8(x[j][0] * FP8_SH, x[j][1] * FP8_SH, x[j][2] * FP8_SH, x[j][3] * FP8_SH); }
.LBB0_1938:
	s_nop 0
	v_and_b32_e32 v121, 0xffff0000, v100
	v_and_b32_e32 v120, 0xffff0000, v98
	v_and_b32_e32 v125, 0xffff0000, v101
	v_and_b32_e32 v124, 0xffff0000, v99
	v_lshlrev_b32_e32 v119, 16, v100
	v_lshlrev_b32_e32 v118, 16, v98
	v_lshlrev_b32_e32 v123, 16, v101
	v_lshlrev_b32_e32 v122, 16, v99
	v_pk_mul_f32 v[134:135], v[120:121], v[120:121]
	v_pk_mul_f32 v[136:137], v[124:125], v[124:125]
	v_pk_fma_f32 v[134:135], v[118:119], v[118:119], v[134:135]
	v_pk_fma_f32 v[136:137], v[122:123], v[122:123], v[136:137]
	v_and_b32_e32 v129, 0xffff0000, v97
	v_and_b32_e32 v128, 0xffff0000, v96
	v_pk_add_f32 v[134:135], v[134:135], v[136:137]
	v_lshlrev_b32_e32 v127, 16, v97
	v_lshlrev_b32_e32 v126, 16, v96
	v_lshlrev_b32_e32 v130, 16, v94
	v_and_b32_e32 v131, 0xffff0000, v94
	v_lshlrev_b32_e32 v132, 16, v95
	v_lshlrev_b32_e32 v100, 16, v92
	v_pk_add_f32 v[134:135], v[134:135], v[134:135] op_sel_hi:[0,1]
	v_pk_mul_f32 v[136:137], v[128:129], v[128:129]
	v_and_b32_e32 v133, 0xffff0000, v95
	v_pk_fma_f32 v[136:137], v[126:127], v[126:127], v[136:137]
	v_mul_f32_e32 v101, v130, v130
	v_mul_f32_e32 v139, v131, v131
	v_mul_f32_e32 v134, v132, v132
	v_mov_b32_e32 v138, v100
	v_and_b32_e32 v117, 0xffff0000, v92
	v_lshlrev_b32_e32 v98, 16, v93
	v_and_b32_e32 v99, 0xffff0000, v93
	v_pk_add_f32 v[136:137], v[136:137], v[136:137] op_sel_hi:[0,1]
	v_pk_fma_f32 v[140:141], v[132:133], v[132:133], v[134:135] op_sel_hi:[1,1,0]
	v_pk_add_f32 v[138:139], v[100:101], v[138:139]
	v_mul_f32_e32 v140, v117, v117
	v_mul_f32_e32 v136, v98, v98
	v_mul_f32_e32 v134, v99, v99
	v_mul_f32_e32 v142, v100, v100
	v_mov_b32_e32 v143, v139
	v_pk_add_f32 v[138:139], v[142:143], v[140:141]
	v_pk_add_f32 v[134:135], v[136:137], v[134:135]
	v_and_b32_e32 v95, 0xffff0000, v91
	v_and_b32_e32 v94, 0xffff0000, v90
	v_pk_add_f32 v[134:135], v[138:139], v[134:135]
	v_lshlrev_b32_e32 v97, 16, v91
	v_lshlrev_b32_e32 v96, 16, v90
	v_lshlrev_b32_e32 v90, 16, v88
	v_and_b32_e32 v91, 0xffff0000, v88
	v_lshlrev_b32_e32 v92, 16, v89
	v_lshlrev_b32_e32 v88, 16, v86
	v_pk_add_f32 v[134:135], v[134:135], v[134:135] op_sel_hi:[0,1]
	v_pk_mul_f32 v[136:137], v[94:95], v[94:95]
	v_and_b32_e32 v93, 0xffff0000, v89
	v_pk_fma_f32 v[136:137], v[96:97], v[96:97], v[136:137]
	v_mul_f32_e32 v89, v90, v90
	v_mul_f32_e32 v139, v91, v91
	v_mul_f32_e32 v134, v92, v92
	v_mov_b32_e32 v138, v88
	v_and_b32_e32 v152, 0xffff0000, v86
	v_lshlrev_b32_e32 v86, 16, v87
	v_and_b32_e32 v87, 0xffff0000, v87
	v_pk_add_f32 v[136:137], v[136:137], v[136:137] op_sel_hi:[0,1]
	v_pk_fma_f32 v[140:141], v[92:93], v[92:93], v[134:135] op_sel_hi:[1,1,0]
	v_pk_add_f32 v[138:139], v[88:89], v[138:139]
	v_mul_f32_e32 v140, v152, v152
	v_mul_f32_e32 v136, v86, v86
	v_mul_f32_e32 v134, v87, v87
	v_mul_f32_e32 v142, v88, v88
	v_mov_b32_e32 v143, v139
	v_pk_add_f32 v[138:139], v[142:143], v[140:141]
	v_pk_add_f32 v[134:135], v[136:137], v[134:135]
	v_mov_b32_e32 v142, 0
	v_pk_add_f32 v[134:135], v[138:139], v[134:135]
	v_mov_b32_e32 v138, v122
	v_add_f32_e32 v89, v134, v135
	v_mov_b32_e32 v139, v124
	v_mov_b32_e32 v124, v123
	v_mov_b32_e32 v143, 0
	v_lshl_add_u64 v[140:141], s[2:3], 0, v[82:83]
	v_add_f32_dpp v101, v89, v89 quad_perm:[1,0,3,2] row_mask:0xf bank_mask:0xf
	s_nop 1
	v_add_f32_dpp v89, v101, v101 quad_perm:[2,3,0,1] row_mask:0xf bank_mask:0xf
	s_nop 1
	v_mov_b32_dpp v101, v89 row_half_mirror row_mask:0xf bank_mask:0xf
	s_nop 1
	v_add_f32_dpp v89, v101, v89 quad_perm:[3,2,1,0] row_mask:0xf bank_mask:0xf
	s_nop 1
	v_add_f32_dpp v101, v89, v89 row_ror:8 row_mask:0xf bank_mask:0xf
	v_mov_b32_e32 v89, v101
	s_nop 1
	v_permlane16_swap_b32_e32 v101, v89
	v_add_f32_e32 v89, v101, v89
	v_mov_b32_e32 v101, v89
	s_nop 1
	v_permlane32_swap_b32_e32 v89, v101
	v_add_f32_e32 v89, v89, v101
	v_fmamk_f32 v89, v89, 0x3a000000, v114
	v_mul_f32_e32 v101, 0x4f800000, v89
	v_cmp_gt_f32_e32 vcc, s29, v89
	s_nop 1
	v_cndmask_b32_e32 v89, v89, v101, vcc
	v_sqrt_f32_e32 v101, v89
	s_nop 0
	v_add_u32_e32 v134, -1, v101
	v_fma_f32 v135, -v134, v101, v89
	v_cmp_ge_f32_e64 s[14:15], 0, v135
	v_add_u32_e32 v135, 1, v101
	s_nop 0
	v_cndmask_b32_e64 v134, v101, v134, s[14:15]
	v_fma_f32 v101, -v135, v101, v89
	v_cmp_lt_f32_e64 s[14:15], 0, v101
	s_nop 1
	v_cndmask_b32_e64 v101, v134, v135, s[14:15]
	v_mul_f32_e32 v134, 0x37800000, v101
	v_cndmask_b32_e32 v101, v101, v134, vcc
	v_cmp_class_f32_e32 vcc, v89, v115
	s_nop 1
	v_cndmask_b32_e32 v89, v101, v89, vcc
	v_div_scale_f32 v101, s[0:1], v89, v89, 1.0
	v_rcp_f32_e32 v134, v101
	s_nop 0
	v_fma_f32 v135, -v101, v134, 1.0
	v_fmac_f32_e32 v134, v135, v134
	v_div_scale_f32 v135, vcc, 1.0, v89, 1.0
	v_mul_f32_e32 v136, v135, v134
	v_fma_f32 v137, -v101, v136, v135
	v_fmac_f32_e32 v136, v137, v134
	v_fma_f32 v101, -v101, v136, v135
	v_div_fmas_f32 v101, v101, v134, v136
	v_div_fixup_f32 v134, v101, v89, 1.0
	v_mov_b32_e32 v136, v118
	v_mov_b32_e32 v137, v120
	v_pk_mul_f32 v[136:137], v[136:137], v[134:135] op_sel_hi:[1,0]
	v_pk_mul_f32 v[138:139], v[138:139], v[134:135] op_sel_hi:[1,0]
	v_pk_fma_f32 v[136:137], v[34:35], v[136:137], v[2:3]
	v_mov_b32_e32 v135, 0
	v_mul_f32_e32 v89, 0x41800000, v136
	v_mul_f32_e32 v101, 0x41800000, v137
	v_med3_f32 v89, v89, s30, v116
	v_med3_f32 v101, v101, s30, v116
	v_cvt_pk_fp8_f32 v135, v89, v101
	v_pk_fma_f32 v[138:139], v[36:37], v[138:139], v[4:5]
	v_mov_b32_e32 v120, v119
	v_mul_f32_e32 v118, 0x41800000, v138
	v_mul_f32_e32 v89, 0x41800000, v139
	v_med3_f32 v101, v118, s30, v116
	v_med3_f32 v89, v89, s30, v116
	v_cvt_pk_fp8_f32 v135, v101, v89 op_sel:[0,0,1]
	v_add_co_u32_e32 v140, vcc, s31, v140
	v_pk_mul_f32 v[118:119], v[120:121], v[134:135] op_sel_hi:[1,0]
; #define GAS __attribute__((address_space(1)))
; #define LAS __attribute__((address_space(3)))
; __device__ __forceinline__ unsigned cvt_pk_bf16(float lo, float hi) { unsigned r; asm volatile("v_cvt_pk_bf16_f32 %0, %1, %2" : "=v"(r) : "v"(lo), "v"(hi)); return r; }
; __device__ __forceinline__ void phase_norm2(Frame& F, int l) {
;     ...
;         for (int j = 0; j < 8; ++j) { const int c = j * 256 + 4 * F.lane;
;             x[j] = x[j] * rs * ga[j] + sb[j]; *(GAS unsigned*)(ho + c) = pk4_fp8(x[j][0] * FP8_SH, x[j][1] * FP8_SH, x[j][2] * FP8_SH, x[j][3] * FP8_SH); }
;         typedef __bf16 bf2_t __attribute__((ext_vector_type(2)));
;         unsigned xb[8][2];
; #pragma unroll
;         for (int j = 0; j < 8; ++j) { xb[j][0] = pg8::cvt_pk_bf16(x[j][0], x[j][1]); xb[j][1] = pg8::cvt_pk_bf16(x[j][2], x[j][3]); }
;     ...
;                 const v2u w0 = *(const LAS v2u*)(rwt + eg * DM + o), w1 = *(const LAS v2u*)(rwt + (eg + 1) * DM + o), w2 = *(const LAS v2u*)(rwt + (eg + 2) * DM + o), w3 = *(const LAS v2u*)(rwt + (eg + 3) * DM + o);
	v_pk_mul_f32 v[120:121], v[124:125], v[134:135] op_sel_hi:[1,0]
	v_pk_fma_f32 v[124:125], v[38:39], v[118:119], v[6:7]
	v_pk_fma_f32 v[122:123], v[40:41], v[120:121], v[8:9]
	v_mul_f32_e32 v89, 0x41800000, v124
	v_mul_f32_e32 v101, 0x41800000, v125
	v_med3_f32 v89, v89, s30, v116
	v_med3_f32 v101, v101, s30, v116
	v_mul_f32_e32 v118, 0x41800000, v122
	v_cvt_pk_fp8_f32 v142, v89, v101
	v_med3_f32 v101, v118, s30, v116
	v_mov_b32_e32 v118, v126
	v_mov_b32_e32 v119, v128
	v_mul_f32_e32 v89, 0x41800000, v123
	v_pk_mul_f32 v[118:119], v[134:135], v[118:119] op_sel_hi:[0,1]
	v_mov_b32_e32 v128, v127
	v_med3_f32 v89, v89, s30, v116
	v_pk_mul_f32 v[120:121], v[134:135], v[128:129] op_sel_hi:[0,1]
	v_pk_fma_f32 v[128:129], v[42:43], v[118:119], v[10:11]
	v_cvt_pk_fp8_f32 v142, v101, v89 op_sel:[0,0,1]
	v_mul_f32_e32 v89, 0x41800000, v128
	v_mul_f32_e32 v101, 0x41800000, v129
	v_med3_f32 v89, v89, s30, v116
	v_med3_f32 v101, v101, s30, v116
	v_pk_fma_f32 v[126:127], v[44:45], v[120:121], v[12:13]
	v_cvt_pk_fp8_f32 v143, v89, v101
	v_mul_f32_e32 v118, 0x41800000, v126
	v_mul_f32_e32 v89, 0x41800000, v127
	v_med3_f32 v101, v118, s30, v116
	v_pk_mul_f32 v[118:119], v[130:131], v[134:135] op_sel_hi:[1,0]
	v_med3_f32 v89, v89, s30, v116
	v_pk_mul_f32 v[120:121], v[132:133], v[134:135] op_sel_hi:[1,0]
	v_pk_fma_f32 v[132:133], v[46:47], v[118:119], v[14:15]
	v_cvt_pk_fp8_f32 v143, v101, v89 op_sel:[0,0,1]
	v_mul_f32_e32 v89, 0x41800000, v132
	v_mul_f32_e32 v101, 0x41800000, v133
	v_med3_f32 v89, v89, s30, v116
	v_med3_f32 v101, v101, s30, v116
	v_mov_b32_e32 v119, 0
	v_cvt_pk_fp8_f32 v119, v89, v101
	v_pk_fma_f32 v[130:131], v[48:49], v[120:121], v[16:17]
	v_addc_co_u32_e32 v141, vcc, 0, v141, vcc
	v_mul_f32_e32 v118, 0x41800000, v130
	v_mul_f32_e32 v89, 0x41800000, v131
	v_med3_f32 v101, v118, s30, v116
	v_med3_f32 v89, v89, s30, v116
	v_cvt_pk_fp8_f32 v119, v101, v89 op_sel:[0,0,1]
	v_mov_b32_e32 v101, v117
	v_pk_mul_f32 v[100:101], v[100:101], v[134:135] op_sel_hi:[1,0]
	v_pk_mul_f32 v[98:99], v[98:99], v[134:135] op_sel_hi:[1,0]
	v_pk_fma_f32 v[144:145], v[50:51], v[100:101], v[18:19]
	global_store_dword v[140:141], v135, off
	global_store_dword v[140:141], v142, off offset:256
	global_store_dword v[140:141], v143, off offset:512
	global_store_dword v[140:141], v119, off offset:768
	v_pk_fma_f32 v[142:143], v[52:53], v[98:99], v[20:21]
	v_mul_f32_e32 v89, 0x41800000, v144
	v_mul_f32_e32 v98, 0x41800000, v145
	v_med3_f32 v89, v89, s30, v116
	v_med3_f32 v98, v98, s30, v116
	v_mov_b32_e32 v100, 0
	v_cvt_pk_fp8_f32 v100, v89, v98
	v_mul_f32_e32 v99, 0x41800000, v142
	v_mul_f32_e32 v89, 0x41800000, v143
	v_med3_f32 v98, v99, s30, v116
	v_med3_f32 v89, v89, s30, v116
	v_cvt_pk_fp8_f32 v100, v98, v89 op_sel:[0,0,1]
	v_mov_b32_e32 v98, v96
	v_mov_b32_e32 v99, v94
	v_pk_mul_f32 v[98:99], v[134:135], v[98:99] op_sel_hi:[0,1]
	v_mov_b32_e32 v94, v97
	v_pk_mul_f32 v[94:95], v[134:135], v[94:95] op_sel_hi:[0,1]
	v_pk_fma_f32 v[146:147], v[54:55], v[98:99], v[22:23]
	v_pk_fma_f32 v[96:97], v[56:57], v[94:95], v[24:25]
	v_mul_f32_e32 v89, 0x41800000, v146
	v_mul_f32_e32 v94, 0x41800000, v147
	v_med3_f32 v89, v89, s30, v116
	v_med3_f32 v94, v94, s30, v116
	v_mov_b32_e32 v98, 0
	v_cvt_pk_fp8_f32 v98, v89, v94
	v_mul_f32_e32 v95, 0x41800000, v96
	v_mul_f32_e32 v89, 0x41800000, v97
	v_pk_mul_f32 v[90:91], v[90:91], v[134:135] op_sel_hi:[1,0]
	v_med3_f32 v94, v95, s30, v116
	v_med3_f32 v89, v89, s30, v116
	v_pk_fma_f32 v[150:151], v[58:59], v[90:91], v[26:27]
	v_cvt_pk_fp8_f32 v98, v94, v89 op_sel:[0,0,1]
	v_pk_mul_f32 v[92:93], v[92:93], v[134:135] op_sel_hi:[1,0]
	v_mul_f32_e32 v89, 0x41800000, v150
	v_mul_f32_e32 v90, 0x41800000, v151
	v_pk_fma_f32 v[148:149], v[60:61], v[92:93], v[28:29]
	v_med3_f32 v89, v89, s30, v116
	v_med3_f32 v90, v90, s30, v116
	v_mov_b32_e32 v92, 0
	v_cvt_pk_fp8_f32 v92, v89, v90
	v_mul_f32_e32 v91, 0x41800000, v148
	v_mul_f32_e32 v89, 0x41800000, v149
	v_med3_f32 v90, v91, s30, v116
	v_med3_f32 v89, v89, s30, v116
	v_cvt_pk_fp8_f32 v92, v90, v89 op_sel:[0,0,1]
	v_mov_b32_e32 v89, v152
	v_pk_mul_f32 v[88:89], v[88:89], v[134:135] op_sel_hi:[1,0]
	v_pk_mul_f32 v[86:87], v[86:87], v[134:135] op_sel_hi:[1,0]
	v_mov_b32_e32 v91, 0
	v_pk_fma_f32 v[134:135], v[64:65], v[86:87], v[32:33]
	v_pk_fma_f32 v[86:87], v[62:63], v[88:89], v[30:31]
	v_mul_f32_e32 v90, 0x41800000, v134
	v_mul_f32_e32 v88, 0x41800000, v86
	v_mul_f32_e32 v89, 0x41800000, v87
	v_med3_f32 v88, v88, s30, v116
	v_med3_f32 v89, v89, s30, v116
	v_cvt_pk_fp8_f32 v91, v88, v89
	v_mul_f32_e32 v88, 0x41800000, v135
	v_med3_f32 v89, v90, s30, v116
	v_med3_f32 v88, v88, s30, v116
	v_cvt_pk_fp8_f32 v91, v89, v88 op_sel:[0,0,1]
	global_store_dword v[140:141], v100, off offset:1024
	global_store_dword v[140:141], v98, off offset:1280
	global_store_dword v[140:141], v92, off offset:1536
	global_store_dword v[140:141], v91, off offset:1792
	v_cvt_pk_bf16_f32 v166, v136, v137
	v_cvt_pk_bf16_f32 v167, v138, v139
	v_cvt_pk_bf16_f32 v168, v124, v125
	v_cvt_pk_bf16_f32 v169, v122, v123
	v_cvt_pk_bf16_f32 v170, v128, v129
	v_cvt_pk_bf16_f32 v171, v126, v127
	v_cvt_pk_bf16_f32 v172, v132, v133
	v_cvt_pk_bf16_f32 v173, v130, v131
	v_cvt_pk_bf16_f32 v174, v144, v145
	v_cvt_pk_bf16_f32 v175, v142, v143
	v_cvt_pk_bf16_f32 v176, v146, v147
	v_cvt_pk_bf16_f32 v177, v96, v97
	v_cvt_pk_bf16_f32 v178, v150, v151
	v_cvt_pk_bf16_f32 v179, v148, v149
	v_cvt_pk_bf16_f32 v180, v86, v87
	v_cvt_pk_bf16_f32 v181, v134, v135
	ds_read2st64_b64 v[122:125], v107 offset1:1
	ds_read2st64_b64 v[126:129], v107 offset0:8 offset1:9
	ds_read2st64_b64 v[130:133], v107 offset0:16 offset1:17
	ds_read2st64_b64 v[134:137], v107 offset0:24 offset1:25
	v_mov_b32_e32 v88, 0
	ds_read2st64_b64 v[138:141], v107 offset0:2 offset1:3
	ds_read2st64_b64 v[142:145], v107 offset0:10 offset1:11
	s_waitcnt lgkmcnt(5)
; #define LAS __attribute__((address_space(3)))
; __device__ __forceinline__ void phase_norm2(Frame& F, int l) {
;     ...
;         for (int eg = 0; eg < NE; eg += 4) { float s0 = 0.f, s1 = 0.f, s2 = 0.f, s3 = 0.f;
; #pragma unroll
;             for (int j = 0; j < 8; ++j) { const int o = j * 256 + 4 * F.lane;
;                 const v2u w0 = *(const LAS v2u*)(rwt + eg * DM + o), w1 = *(const LAS v2u*)(rwt + (eg + 1) * DM + o), w2 = *(const LAS v2u*)(rwt + (eg + 2) * DM + o), w3 = *(const LAS v2u*)(rwt + (eg + 3) * DM + o);
;                 const unsigned w0x = w0.x, w0y = w0.y, w1x = w1.x, w1y = w1.y, w2x = w2.x, w2y = w2.y, w3x = w3.x, w3y = w3.y, xlo = xb[j][0], xhi = xb[j][1];
;                 const bf2_t xl = __builtin_bit_cast(bf2_t, xlo), xh = __builtin_bit_cast(bf2_t, xhi);
;                 s0 = __builtin_amdgcn_fdot2_f32_bf16(xl, __builtin_bit_cast(bf2_t, w0x), s0, false); s0 = __builtin_amdgcn_fdot2_f32_bf16(xh, __builtin_bit_cast(bf2_t, w0y), s0, false);
;                 s1 = __builtin_amdgcn_fdot2_f32_bf16(xl, __builtin_bit_cast(bf2_t, w1x), s1, false); s1 = __builtin_amdgcn_fdot2_f32_bf16(xh, __builtin_bit_cast(bf2_t, w1y), s1, false);
;                 s2 = __builtin_amdgcn_fdot2_f32_bf16(xl, __builtin_bit_cast(bf2_t, w2x), s2, false); s2 = __builtin_amdgcn_fdot2_f32_bf16(xh, __builtin_bit_cast(bf2_t, w2y), s2, false);
;                 s3 = __builtin_amdgcn_fdot2_f32_bf16(xl, __builtin_bit_cast(bf2_t, w3x), s3, false); s3 = __builtin_amdgcn_fdot2_f32_bf16(xh, __builtin_bit_cast(bf2_t, w3y), s3, false); }
;             p[eg] = s0; p[eg + 1] = s1; p[eg + 2] = s2; p[eg + 3] = s3; __builtin_amdgcn_sched_barrier(0); }
	v_mfma_f32_4x4x4_16b_bf16 v[182:185], v[122:123], v[166:167], 0
	v_mov_b32_e32 v93, 0
	v_mov_b32_e32 v96, 0
	ds_read2st64_b64 v[146:149], v107 offset0:18 offset1:19
	ds_read2st64_b64 v[150:153], v107 offset0:26 offset1:27
	v_mov_b32_e32 v97, 0
	v_mfma_f32_4x4x4_16b_bf16 v[182:185], v[124:125], v[168:169], v[182:185]
	s_waitcnt lgkmcnt(6)
	v_mfma_f32_4x4x4_16b_bf16 v[186:189], v[126:127], v[166:167], 0
	s_waitcnt lgkmcnt(5)
	v_mfma_f32_4x4x4_16b_bf16 v[190:193], v[130:131], v[166:167], 0
	s_waitcnt lgkmcnt(4)
	v_mfma_f32_4x4x4_16b_bf16 v[194:197], v[134:135], v[166:167], 0
	s_waitcnt lgkmcnt(3)
	v_mfma_f32_4x4x4_16b_bf16 v[182:185], v[138:139], v[170:171], v[182:185]
	v_mfma_f32_4x4x4_16b_bf16 v[186:189], v[128:129], v[168:169], v[186:189]
	v_mfma_f32_4x4x4_16b_bf16 v[190:193], v[132:133], v[168:169], v[190:193]
	v_mfma_f32_4x4x4_16b_bf16 v[194:197], v[136:137], v[168:169], v[194:197]
	v_mfma_f32_4x4x4_16b_bf16 v[182:185], v[140:141], v[172:173], v[182:185]
	s_waitcnt lgkmcnt(2)
	v_mfma_f32_4x4x4_16b_bf16 v[186:189], v[142:143], v[170:171], v[186:189]
	s_waitcnt lgkmcnt(1)
	v_mfma_f32_4x4x4_16b_bf16 v[190:193], v[146:147], v[170:171], v[190:193]
	s_waitcnt lgkmcnt(0)
	v_mfma_f32_4x4x4_16b_bf16 v[194:197], v[150:151], v[170:171], v[194:197]
	ds_read2st64_b64 v[122:125], v107 offset0:4 offset1:5
	ds_read2st64_b64 v[126:129], v107 offset0:12 offset1:13
	ds_read2st64_b64 v[130:133], v107 offset0:20 offset1:21
	ds_read2st64_b64 v[134:137], v107 offset0:28 offset1:29
	ds_read2st64_b64 v[138:141], v107 offset0:6 offset1:7
	v_mfma_f32_4x4x4_16b_bf16 v[186:189], v[144:145], v[172:173], v[186:189]
	v_mfma_f32_4x4x4_16b_bf16 v[190:193], v[148:149], v[172:173], v[190:193]
	v_mfma_f32_4x4x4_16b_bf16 v[194:197], v[152:153], v[172:173], v[194:197]
	s_waitcnt lgkmcnt(4)
	v_mfma_f32_4x4x4_16b_bf16 v[182:185], v[122:123], v[174:175], v[182:185]
	ds_read2st64_b64 v[142:145], v107 offset0:14 offset1:15
	ds_read2st64_b64 v[146:149], v107 offset0:22 offset1:23
	ds_read2st64_b64 v[150:153], v107 offset0:30 offset1:31
	s_waitcnt lgkmcnt(6)
	v_mfma_f32_4x4x4_16b_bf16 v[186:189], v[126:127], v[174:175], v[186:189]
	s_waitcnt lgkmcnt(5)
	v_mfma_f32_4x4x4_16b_bf16 v[190:193], v[130:131], v[174:175], v[190:193]
	s_waitcnt lgkmcnt(4)
	v_mfma_f32_4x4x4_16b_bf16 v[194:197], v[134:135], v[174:175], v[194:197]
	v_mfma_f32_4x4x4_16b_bf16 v[182:185], v[124:125], v[176:177], v[182:185]
	v_mfma_f32_4x4x4_16b_bf16 v[186:189], v[128:129], v[176:177], v[186:189]
	v_mfma_f32_4x4x4_16b_bf16 v[190:193], v[132:133], v[176:177], v[190:193]
	v_mfma_f32_4x4x4_16b_bf16 v[194:197], v[136:137], v[176:177], v[194:197]
	s_waitcnt lgkmcnt(3)
	v_mfma_f32_4x4x4_16b_bf16 v[182:185], v[138:139], v[178:179], v[182:185]
	s_waitcnt lgkmcnt(2)
	v_mfma_f32_4x4x4_16b_bf16 v[186:189], v[142:143], v[178:179], v[186:189]
	s_waitcnt lgkmcnt(1)
	v_mfma_f32_4x4x4_16b_bf16 v[190:193], v[146:147], v[178:179], v[190:193]
	s_waitcnt lgkmcnt(0)
	v_mfma_f32_4x4x4_16b_bf16 v[194:197], v[150:151], v[178:179], v[194:197]
	v_mfma_f32_4x4x4_16b_bf16 v[182:185], v[140:141], v[180:181], v[182:185]
	v_mfma_f32_4x4x4_16b_bf16 v[186:189], v[144:145], v[180:181], v[186:189]
	v_mfma_f32_4x4x4_16b_bf16 v[190:193], v[148:149], v[180:181], v[190:193]
	v_mfma_f32_4x4x4_16b_bf16 v[194:197], v[152:153], v[180:181], v[194:197]
	s_mov_b32 s98, 0x22222222
	s_mov_b32 s99, 0x22222222
	s_mov_b32 s100, 0x44444444
	s_mov_b32 s101, 0x44444444
	s_mov_b32 vcc_lo, 0x88888888
	s_mov_b32 vcc_hi, 0x88888888
	s_nop 4
	v_cndmask_b32_e64 v88, v182, v183, s[98:99]
	v_cndmask_b32_e64 v88, v88, v184, s[100:101]
	v_cndmask_b32_e32 v88, v88, v185, vcc
	v_cndmask_b32_e64 v93, v186, v187, s[98:99]
	v_cndmask_b32_e64 v93, v93, v188, s[100:101]
	v_cndmask_b32_e32 v93, v93, v189, vcc
	v_cndmask_b32_e64 v96, v190, v191, s[98:99]
	v_cndmask_b32_e64 v96, v96, v192, s[100:101]
	v_cndmask_b32_e32 v96, v96, v193, vcc
	v_cndmask_b32_e64 v97, v194, v195, s[98:99]
	v_cndmask_b32_e64 v97, v97, v196, s[100:101]
	v_cndmask_b32_e32 v97, v97, v197, vcc
	ds_read2st64_b64 v[124:127], v107 offset0:32 offset1:33
	ds_read2st64_b64 v[128:131], v107 offset0:40 offset1:41
	ds_read2st64_b64 v[132:135], v107 offset0:48 offset1:49
	ds_read2st64_b64 v[136:139], v107 offset0:56 offset1:57
	v_mov_b32_e32 v121, 0
	ds_read2st64_b64 v[140:143], v107 offset0:34 offset1:35
	ds_read2st64_b64 v[144:147], v107 offset0:42 offset1:43
	s_waitcnt lgkmcnt(5)
	v_mfma_f32_4x4x4_16b_bf16 v[218:221], v[124:125], v[166:167], 0
	v_mov_b32_e32 v123, 0
	s_waitcnt lgkmcnt(4)
	v_mfma_f32_4x4x4_16b_bf16 v[222:225], v[128:129], v[166:167], 0
	v_mov_b32_e32 v124, 0
	ds_read2st64_b64 v[148:151], v107 offset0:50 offset1:51
	ds_read2st64_b64 v[152:155], v107 offset0:58 offset1:59
	v_mov_b32_e32 v122, 0
	v_mfma_f32_4x4x4_16b_bf16 v[218:221], v[126:127], v[168:169], v[218:221]
	s_waitcnt lgkmcnt(5)
	v_mfma_f32_4x4x4_16b_bf16 v[226:229], v[132:133], v[166:167], 0
	s_waitcnt lgkmcnt(4)
	v_mfma_f32_4x4x4_16b_bf16 v[230:233], v[136:137], v[166:167], 0
	v_mfma_f32_4x4x4_16b_bf16 v[222:225], v[130:131], v[168:169], v[222:225]
	s_waitcnt lgkmcnt(3)
	v_mfma_f32_4x4x4_16b_bf16 v[218:221], v[140:141], v[170:171], v[218:221]
	v_mfma_f32_4x4x4_16b_bf16 v[226:229], v[134:135], v[168:169], v[226:229]
	v_mfma_f32_4x4x4_16b_bf16 v[230:233], v[138:139], v[168:169], v[230:233]
	s_waitcnt lgkmcnt(2)
	v_mfma_f32_4x4x4_16b_bf16 v[222:225], v[144:145], v[170:171], v[222:225]
	v_mfma_f32_4x4x4_16b_bf16 v[218:221], v[142:143], v[172:173], v[218:221]
	s_waitcnt lgkmcnt(1)
	v_mfma_f32_4x4x4_16b_bf16 v[226:229], v[148:149], v[170:171], v[226:229]
	s_waitcnt lgkmcnt(0)
; #define LAS __attribute__((address_space(3)))
; __device__ __forceinline__ void phase_norm2(Frame& F, int l) {
;     ...
;         for (int eg = 0; eg < NE; eg += 4) { float s0 = 0.f, s1 = 0.f, s2 = 0.f, s3 = 0.f;
; #pragma unroll
;             for (int j = 0; j < 8; ++j) { const int o = j * 256 + 4 * F.lane;
;                 const v2u w0 = *(const LAS v2u*)(rwt + eg * DM + o), w1 = *(const LAS v2u*)(rwt + (eg + 1) * DM + o), w2 = *(const LAS v2u*)(rwt + (eg + 2) * DM + o), w3 = *(const LAS v2u*)(rwt + (eg + 3) * DM + o);
;                 const unsigned w0x = w0.x, w0y = w0.y, w1x = w1.x, w1y = w1.y, w2x = w2.x, w2y = w2.y, w3x = w3.x, w3y = w3.y, xlo = xb[j][0], xhi = xb[j][1];
;                 const bf2_t xl = __builtin_bit_cast(bf2_t, xlo), xh = __builtin_bit_cast(bf2_t, xhi);
;                 s0 = __builtin_amdgcn_fdot2_f32_bf16(xl, __builtin_bit_cast(bf2_t, w0x), s0, false); s0 = __builtin_amdgcn_fdot2_f32_bf16(xh, __builtin_bit_cast(bf2_t, w0y), s0, false);
;                 s1 = __builtin_amdgcn_fdot2_f32_bf16(xl, __builtin_bit_cast(bf2_t, w1x), s1, false); s1 = __builtin_amdgcn_fdot2_f32_bf16(xh, __builtin_bit_cast(bf2_t, w1y), s1, false);
;                 s2 = __builtin_amdgcn_fdot2_f32_bf16(xl, __builtin_bit_cast(bf2_t, w2x), s2, false); s2 = __builtin_amdgcn_fdot2_f32_bf16(xh, __builtin_bit_cast(bf2_t, w2y), s2, false);
;                 s3 = __builtin_amdgcn_fdot2_f32_bf16(xl, __builtin_bit_cast(bf2_t, w3x), s3, false); s3 = __builtin_amdgcn_fdot2_f32_bf16(xh, __builtin_bit_cast(bf2_t, w3y), s3, false); }
;             p[eg] = s0; p[eg + 1] = s1; p[eg + 2] = s2; p[eg + 3] = s3; __builtin_amdgcn_sched_barrier(0); }
	v_mfma_f32_4x4x4_16b_bf16 v[230:233], v[152:153], v[170:171], v[230:233]
	ds_read2st64_b64 v[126:129], v107 offset0:36 offset1:37
	ds_read2st64_b64 v[130:133], v107 offset0:44 offset1:45
	ds_read2st64_b64 v[134:137], v107 offset0:52 offset1:53
	ds_read2st64_b64 v[138:141], v107 offset0:60 offset1:61
	ds_read2st64_b64 v[142:145], v107 offset0:38 offset1:39
	v_mfma_f32_4x4x4_16b_bf16 v[222:225], v[146:147], v[172:173], v[222:225]
	v_mfma_f32_4x4x4_16b_bf16 v[226:229], v[150:151], v[172:173], v[226:229]
	v_mfma_f32_4x4x4_16b_bf16 v[230:233], v[154:155], v[172:173], v[230:233]
	ds_read2st64_b64 v[146:149], v107 offset0:46 offset1:47
	ds_read2st64_b64 v[150:153], v107 offset0:54 offset1:55
	ds_read2st64_b64 v[154:157], v107 offset0:62 offset1:63
	s_waitcnt lgkmcnt(7)
	v_mfma_f32_4x4x4_16b_bf16 v[218:221], v[126:127], v[174:175], v[218:221]
	s_waitcnt lgkmcnt(6)
	v_mfma_f32_4x4x4_16b_bf16 v[222:225], v[130:131], v[174:175], v[222:225]
	s_waitcnt lgkmcnt(5)
	v_mfma_f32_4x4x4_16b_bf16 v[226:229], v[134:135], v[174:175], v[226:229]
	s_waitcnt lgkmcnt(4)
	v_mfma_f32_4x4x4_16b_bf16 v[230:233], v[138:139], v[174:175], v[230:233]
	v_mfma_f32_4x4x4_16b_bf16 v[218:221], v[128:129], v[176:177], v[218:221]
	v_mfma_f32_4x4x4_16b_bf16 v[222:225], v[132:133], v[176:177], v[222:225]
	v_mfma_f32_4x4x4_16b_bf16 v[226:229], v[136:137], v[176:177], v[226:229]
	v_mfma_f32_4x4x4_16b_bf16 v[230:233], v[140:141], v[176:177], v[230:233]
	s_waitcnt lgkmcnt(3)
	v_mfma_f32_4x4x4_16b_bf16 v[218:221], v[142:143], v[178:179], v[218:221]
	s_waitcnt lgkmcnt(2)
	v_mfma_f32_4x4x4_16b_bf16 v[222:225], v[146:147], v[178:179], v[222:225]
	s_waitcnt lgkmcnt(1)
	v_mfma_f32_4x4x4_16b_bf16 v[226:229], v[150:151], v[178:179], v[226:229]
	s_waitcnt lgkmcnt(0)
	v_mfma_f32_4x4x4_16b_bf16 v[230:233], v[154:155], v[178:179], v[230:233]
	v_mfma_f32_4x4x4_16b_bf16 v[218:221], v[144:145], v[180:181], v[218:221]
	v_mfma_f32_4x4x4_16b_bf16 v[222:225], v[148:149], v[180:181], v[222:225]
	v_mfma_f32_4x4x4_16b_bf16 v[226:229], v[152:153], v[180:181], v[226:229]
	v_mfma_f32_4x4x4_16b_bf16 v[230:233], v[156:157], v[180:181], v[230:233]
	s_mov_b32 s98, 0x22222222
	s_mov_b32 s99, 0x22222222
	s_mov_b32 s100, 0x44444444
	s_mov_b32 s101, 0x44444444
	s_mov_b32 vcc_lo, 0x88888888
	s_mov_b32 vcc_hi, 0x88888888
	s_nop 4
	v_cndmask_b32_e64 v121, v218, v219, s[98:99]
	v_cndmask_b32_e64 v121, v121, v220, s[100:101]
	v_cndmask_b32_e32 v121, v121, v221, vcc
	v_cndmask_b32_e64 v123, v222, v223, s[98:99]
	v_cndmask_b32_e64 v123, v123, v224, s[100:101]
	v_cndmask_b32_e32 v123, v123, v225, vcc
	v_cndmask_b32_e64 v124, v226, v227, s[98:99]
	v_cndmask_b32_e64 v124, v124, v228, s[100:101]
	v_cndmask_b32_e32 v124, v124, v229, vcc
	v_cndmask_b32_e64 v122, v230, v231, s[98:99]
	v_cndmask_b32_e64 v122, v122, v232, s[100:101]
	v_cndmask_b32_e32 v122, v122, v233, vcc
	ds_read2st64_b64 v[126:129], v107 offset0:64 offset1:65
	ds_read2st64_b64 v[130:133], v107 offset0:72 offset1:73
	ds_read2st64_b64 v[134:137], v107 offset0:80 offset1:81
	ds_read2st64_b64 v[138:141], v107 offset0:88 offset1:89
	v_mov_b32_e32 v125, 0
	ds_read2st64_b64 v[142:145], v107 offset0:66 offset1:67
	ds_read2st64_b64 v[146:149], v107 offset0:74 offset1:75
	s_waitcnt lgkmcnt(5)
	v_mfma_f32_4x4x4_16b_bf16 v[182:185], v[126:127], v[166:167], 0
	v_mov_b32_e32 v158, 0
	v_mov_b32_e32 v159, 0
	ds_read2st64_b64 v[150:153], v107 offset0:82 offset1:83
	ds_read2st64_b64 v[154:157], v107 offset0:90 offset1:91
	v_mov_b32_e32 v160, 0
	v_mfma_f32_4x4x4_16b_bf16 v[182:185], v[128:129], v[168:169], v[182:185]
	s_waitcnt lgkmcnt(6)
	v_mfma_f32_4x4x4_16b_bf16 v[186:189], v[130:131], v[166:167], 0
	s_waitcnt lgkmcnt(5)
	v_mfma_f32_4x4x4_16b_bf16 v[190:193], v[134:135], v[166:167], 0
	s_waitcnt lgkmcnt(4)
	v_mfma_f32_4x4x4_16b_bf16 v[194:197], v[138:139], v[166:167], 0
	s_waitcnt lgkmcnt(3)
	v_mfma_f32_4x4x4_16b_bf16 v[182:185], v[142:143], v[170:171], v[182:185]
	v_mfma_f32_4x4x4_16b_bf16 v[186:189], v[132:133], v[168:169], v[186:189]
	v_mfma_f32_4x4x4_16b_bf16 v[190:193], v[136:137], v[168:169], v[190:193]
	v_mfma_f32_4x4x4_16b_bf16 v[194:197], v[140:141], v[168:169], v[194:197]
	v_mfma_f32_4x4x4_16b_bf16 v[182:185], v[144:145], v[172:173], v[182:185]
	s_waitcnt lgkmcnt(2)
	v_mfma_f32_4x4x4_16b_bf16 v[186:189], v[146:147], v[170:171], v[186:189]
	s_waitcnt lgkmcnt(1)
	v_mfma_f32_4x4x4_16b_bf16 v[190:193], v[150:151], v[170:171], v[190:193]
	s_waitcnt lgkmcnt(0)
	v_mfma_f32_4x4x4_16b_bf16 v[194:197], v[154:155], v[170:171], v[194:197]
	ds_read2st64_b64 v[126:129], v107 offset0:68 offset1:69
	ds_read2st64_b64 v[130:133], v107 offset0:76 offset1:77
	ds_read2st64_b64 v[134:137], v107 offset0:84 offset1:85
	ds_read2st64_b64 v[138:141], v107 offset0:92 offset1:93
	ds_read2st64_b64 v[142:145], v107 offset0:70 offset1:71
	v_mfma_f32_4x4x4_16b_bf16 v[186:189], v[148:149], v[172:173], v[186:189]
	v_mfma_f32_4x4x4_16b_bf16 v[190:193], v[152:153], v[172:173], v[190:193]
	v_mfma_f32_4x4x4_16b_bf16 v[194:197], v[156:157], v[172:173], v[194:197]
	ds_read2st64_b64 v[146:149], v107 offset0:78 offset1:79
	ds_read2st64_b64 v[150:153], v107 offset0:86 offset1:87
	ds_read2st64_b64 v[154:157], v107 offset0:94 offset1:95
	s_waitcnt lgkmcnt(7)
	v_mfma_f32_4x4x4_16b_bf16 v[182:185], v[126:127], v[174:175], v[182:185]
	s_waitcnt lgkmcnt(6)
	v_mfma_f32_4x4x4_16b_bf16 v[186:189], v[130:131], v[174:175], v[186:189]
	s_waitcnt lgkmcnt(5)
	v_mfma_f32_4x4x4_16b_bf16 v[190:193], v[134:135], v[174:175], v[190:193]
	s_waitcnt lgkmcnt(4)
; #define LAS __attribute__((address_space(3)))
; __device__ __forceinline__ void phase_norm2(Frame& F, int l) {
;     ...
;         for (int eg = 0; eg < NE; eg += 4) { float s0 = 0.f, s1 = 0.f, s2 = 0.f, s3 = 0.f;
; #pragma unroll
;             for (int j = 0; j < 8; ++j) { const int o = j * 256 + 4 * F.lane;
;                 const v2u w0 = *(const LAS v2u*)(rwt + eg * DM + o), w1 = *(const LAS v2u*)(rwt + (eg + 1) * DM + o), w2 = *(const LAS v2u*)(rwt + (eg + 2) * DM + o), w3 = *(const LAS v2u*)(rwt + (eg + 3) * DM + o);
;                 const unsigned w0x = w0.x, w0y = w0.y, w1x = w1.x, w1y = w1.y, w2x = w2.x, w2y = w2.y, w3x = w3.x, w3y = w3.y, xlo = xb[j][0], xhi = xb[j][1];
;                 const bf2_t xl = __builtin_bit_cast(bf2_t, xlo), xh = __builtin_bit_cast(bf2_t, xhi);
;                 s0 = __builtin_amdgcn_fdot2_f32_bf16(xl, __builtin_bit_cast(bf2_t, w0x), s0, false); s0 = __builtin_amdgcn_fdot2_f32_bf16(xh, __builtin_bit_cast(bf2_t, w0y), s0, false);
;                 s1 = __builtin_amdgcn_fdot2_f32_bf16(xl, __builtin_bit_cast(bf2_t, w1x), s1, false); s1 = __builtin_amdgcn_fdot2_f32_bf16(xh, __builtin_bit_cast(bf2_t, w1y), s1, false);
;                 s2 = __builtin_amdgcn_fdot2_f32_bf16(xl, __builtin_bit_cast(bf2_t, w2x), s2, false); s2 = __builtin_amdgcn_fdot2_f32_bf16(xh, __builtin_bit_cast(bf2_t, w2y), s2, false);
;                 s3 = __builtin_amdgcn_fdot2_f32_bf16(xl, __builtin_bit_cast(bf2_t, w3x), s3, false); s3 = __builtin_amdgcn_fdot2_f32_bf16(xh, __builtin_bit_cast(bf2_t, w3y), s3, false); }
;             p[eg] = s0; p[eg + 1] = s1; p[eg + 2] = s2; p[eg + 3] = s3; __builtin_amdgcn_sched_barrier(0); }
	v_mfma_f32_4x4x4_16b_bf16 v[194:197], v[138:139], v[174:175], v[194:197]
	v_mfma_f32_4x4x4_16b_bf16 v[182:185], v[128:129], v[176:177], v[182:185]
	v_mfma_f32_4x4x4_16b_bf16 v[186:189], v[132:133], v[176:177], v[186:189]
	v_mfma_f32_4x4x4_16b_bf16 v[190:193], v[136:137], v[176:177], v[190:193]
	v_mfma_f32_4x4x4_16b_bf16 v[194:197], v[140:141], v[176:177], v[194:197]
	s_waitcnt lgkmcnt(3)
	v_mfma_f32_4x4x4_16b_bf16 v[182:185], v[142:143], v[178:179], v[182:185]
	s_waitcnt lgkmcnt(2)
	v_mfma_f32_4x4x4_16b_bf16 v[186:189], v[146:147], v[178:179], v[186:189]
	s_waitcnt lgkmcnt(1)
	v_mfma_f32_4x4x4_16b_bf16 v[190:193], v[150:151], v[178:179], v[190:193]
	s_waitcnt lgkmcnt(0)
	v_mfma_f32_4x4x4_16b_bf16 v[194:197], v[154:155], v[178:179], v[194:197]
	v_mfma_f32_4x4x4_16b_bf16 v[182:185], v[144:145], v[180:181], v[182:185]
	v_mfma_f32_4x4x4_16b_bf16 v[186:189], v[148:149], v[180:181], v[186:189]
	v_mfma_f32_4x4x4_16b_bf16 v[190:193], v[152:153], v[180:181], v[190:193]
	v_mfma_f32_4x4x4_16b_bf16 v[194:197], v[156:157], v[180:181], v[194:197]
	s_mov_b32 s98, 0x22222222
	s_mov_b32 s99, 0x22222222
	s_mov_b32 s100, 0x44444444
	s_mov_b32 s101, 0x44444444
	s_mov_b32 vcc_lo, 0x88888888
	s_mov_b32 vcc_hi, 0x88888888
	s_nop 4
	v_cndmask_b32_e64 v125, v182, v183, s[98:99]
	v_cndmask_b32_e64 v125, v125, v184, s[100:101]
	v_cndmask_b32_e32 v125, v125, v185, vcc
	v_cndmask_b32_e64 v158, v186, v187, s[98:99]
	v_cndmask_b32_e64 v158, v158, v188, s[100:101]
	v_cndmask_b32_e32 v158, v158, v189, vcc
	v_cndmask_b32_e64 v159, v190, v191, s[98:99]
	v_cndmask_b32_e64 v159, v159, v192, s[100:101]
	v_cndmask_b32_e32 v159, v159, v193, vcc
	v_cndmask_b32_e64 v160, v194, v195, s[98:99]
	v_cndmask_b32_e64 v160, v160, v196, s[100:101]
	v_cndmask_b32_e32 v160, v160, v197, vcc
	ds_read2st64_b64 v[126:129], v107 offset0:96 offset1:97
	ds_read2st64_b64 v[130:133], v107 offset0:104 offset1:105
	ds_read2st64_b64 v[134:137], v107 offset0:112 offset1:113
	ds_read2st64_b64 v[138:141], v107 offset0:120 offset1:121
	v_mov_b32_e32 v161, 0
	ds_read2st64_b64 v[142:145], v107 offset0:98 offset1:99
	ds_read2st64_b64 v[146:149], v107 offset0:106 offset1:107
	v_mov_b32_e32 v162, 0
	v_mov_b32_e32 v163, 0
	ds_read2st64_b64 v[150:153], v107 offset0:114 offset1:115
	ds_read2st64_b64 v[154:157], v107 offset0:122 offset1:123
	v_mov_b32_e32 v164, 0
	s_waitcnt lgkmcnt(7)
	v_mfma_f32_4x4x4_16b_bf16 v[218:221], v[126:127], v[166:167], 0
	s_waitcnt lgkmcnt(6)
	v_mfma_f32_4x4x4_16b_bf16 v[222:225], v[130:131], v[166:167], 0
	s_waitcnt lgkmcnt(5)
	v_mfma_f32_4x4x4_16b_bf16 v[226:229], v[134:135], v[166:167], 0
	s_waitcnt lgkmcnt(4)
	v_mfma_f32_4x4x4_16b_bf16 v[230:233], v[138:139], v[166:167], 0
	v_mfma_f32_4x4x4_16b_bf16 v[218:221], v[128:129], v[168:169], v[218:221]
	v_mfma_f32_4x4x4_16b_bf16 v[222:225], v[132:133], v[168:169], v[222:225]
	v_mfma_f32_4x4x4_16b_bf16 v[226:229], v[136:137], v[168:169], v[226:229]
	v_mfma_f32_4x4x4_16b_bf16 v[230:233], v[140:141], v[168:169], v[230:233]
	s_waitcnt lgkmcnt(3)
	v_mfma_f32_4x4x4_16b_bf16 v[218:221], v[142:143], v[170:171], v[218:221]
	s_waitcnt lgkmcnt(2)
	v_mfma_f32_4x4x4_16b_bf16 v[222:225], v[146:147], v[170:171], v[222:225]
	s_waitcnt lgkmcnt(1)
	v_mfma_f32_4x4x4_16b_bf16 v[226:229], v[150:151], v[170:171], v[226:229]
	s_waitcnt lgkmcnt(0)
	v_mfma_f32_4x4x4_16b_bf16 v[230:233], v[154:155], v[170:171], v[230:233]
	v_mfma_f32_4x4x4_16b_bf16 v[218:221], v[144:145], v[172:173], v[218:221]
	v_mfma_f32_4x4x4_16b_bf16 v[222:225], v[148:149], v[172:173], v[222:225]
	v_mfma_f32_4x4x4_16b_bf16 v[226:229], v[152:153], v[172:173], v[226:229]
	v_mfma_f32_4x4x4_16b_bf16 v[230:233], v[156:157], v[172:173], v[230:233]
	ds_read2st64_b64 v[98:101], v107 offset0:100 offset1:101
	ds_read2st64_b64 v[126:129], v107 offset0:108 offset1:109
	ds_read2st64_b64 v[130:133], v107 offset0:116 offset1:117
	ds_read2st64_b64 v[134:137], v107 offset0:124 offset1:125
	ds_read2st64_b64 v[138:141], v107 offset0:102 offset1:103
	ds_read2st64_b64 v[142:145], v107 offset0:110 offset1:111
	ds_read2st64_b64 v[146:149], v107 offset0:118 offset1:119
	ds_read2st64_b64 v[150:153], v107 offset0:126 offset1:127
	s_waitcnt lgkmcnt(7)
	v_mfma_f32_4x4x4_16b_bf16 v[218:221], v[98:99], v[174:175], v[218:221]
	s_waitcnt lgkmcnt(6)
	v_mfma_f32_4x4x4_16b_bf16 v[222:225], v[126:127], v[174:175], v[222:225]
	s_waitcnt lgkmcnt(5)
	v_mfma_f32_4x4x4_16b_bf16 v[226:229], v[130:131], v[174:175], v[226:229]
	s_waitcnt lgkmcnt(4)
	v_mfma_f32_4x4x4_16b_bf16 v[230:233], v[134:135], v[174:175], v[230:233]
	v_mfma_f32_4x4x4_16b_bf16 v[218:221], v[100:101], v[176:177], v[218:221]
	v_mfma_f32_4x4x4_16b_bf16 v[222:225], v[128:129], v[176:177], v[222:225]
	v_mfma_f32_4x4x4_16b_bf16 v[226:229], v[132:133], v[176:177], v[226:229]
	v_mfma_f32_4x4x4_16b_bf16 v[230:233], v[136:137], v[176:177], v[230:233]
	s_waitcnt lgkmcnt(3)
; __device__ __forceinline__ void phase_norm2(Frame& F, int l) {
;     ...
;         for (int eg = 0; eg < NE; eg += 4) { float s0 = 0.f, s1 = 0.f, s2 = 0.f, s3 = 0.f;
; #pragma unroll
;             for (int j = 0; j < 8; ++j) { const int o = j * 256 + 4 * F.lane;
;                 const v2u w0 = *(const LAS v2u*)(rwt + eg * DM + o), w1 = *(const LAS v2u*)(rwt + (eg + 1) * DM + o), w2 = *(const LAS v2u*)(rwt + (eg + 2) * DM + o), w3 = *(const LAS v2u*)(rwt + (eg + 3) * DM + o);
;                 const unsigned w0x = w0.x, w0y = w0.y, w1x = w1.x, w1y = w1.y, w2x = w2.x, w2y = w2.y, w3x = w3.x, w3y = w3.y, xlo = xb[j][0], xhi = xb[j][1];
;                 const bf2_t xl = __builtin_bit_cast(bf2_t, xlo), xh = __builtin_bit_cast(bf2_t, xhi);
;                 s0 = __builtin_amdgcn_fdot2_f32_bf16(xl, __builtin_bit_cast(bf2_t, w0x), s0, false); s0 = __builtin_amdgcn_fdot2_f32_bf16(xh, __builtin_bit_cast(bf2_t, w0y), s0, false);
;                 s1 = __builtin_amdgcn_fdot2_f32_bf16(xl, __builtin_bit_cast(bf2_t, w1x), s1, false); s1 = __builtin_amdgcn_fdot2_f32_bf16(xh, __builtin_bit_cast(bf2_t, w1y), s1, false);
;                 s2 = __builtin_amdgcn_fdot2_f32_bf16(xl, __builtin_bit_cast(bf2_t, w2x), s2, false); s2 = __builtin_amdgcn_fdot2_f32_bf16(xh, __builtin_bit_cast(bf2_t, w2y), s2, false);
;                 s3 = __builtin_amdgcn_fdot2_f32_bf16(xl, __builtin_bit_cast(bf2_t, w3x), s3, false); s3 = __builtin_amdgcn_fdot2_f32_bf16(xh, __builtin_bit_cast(bf2_t, w3y), s3, false); }
;             p[eg] = s0; p[eg + 1] = s1; p[eg + 2] = s2; p[eg + 3] = s3; __builtin_amdgcn_sched_barrier(0); }
;         const bool b5 = (F.lane & 32) != 0, b4 = (F.lane & 16) != 0, b3 = (F.lane & 8) != 0, b2 = (F.lane & 4) != 0;
;         float q8[8], q4[4], q2[2];
; #pragma unroll
;         for (int i = 0; i < 8; ++i) { const float keep = b5 ? p[i + 8] : p[i], give = b5 ? p[i] : p[i + 8]; q8[i] = keep + __shfl_xor(give, 32); }
; #pragma unroll
;         for (int i = 0; i < 4; ++i) { const float keep = b4 ? q8[i + 4] : q8[i], give = b4 ? q8[i] : q8[i + 4]; q4[i] = keep + __shfl_xor(give, 16); }
; #pragma unroll
;         for (int i = 0; i < 2; ++i) { const float keep = b3 ? q4[i + 2] : q4[i], give = b3 ? q4[i] : q4[i + 2]; q2[i] = keep + __shfl_xor(give, 8); }
;         float lg; { const float keep = b2 ? q2[1] : q2[0], give = b2 ? q2[0] : q2[1]; lg = keep + __shfl_xor(give, 4); }
	v_mfma_f32_4x4x4_16b_bf16 v[218:221], v[138:139], v[178:179], v[218:221]
	s_waitcnt lgkmcnt(2)
	v_mfma_f32_4x4x4_16b_bf16 v[222:225], v[142:143], v[178:179], v[222:225]
	s_waitcnt lgkmcnt(1)
	v_mfma_f32_4x4x4_16b_bf16 v[226:229], v[146:147], v[178:179], v[226:229]
	s_waitcnt lgkmcnt(0)
	v_mfma_f32_4x4x4_16b_bf16 v[230:233], v[150:151], v[178:179], v[230:233]
	v_mfma_f32_4x4x4_16b_bf16 v[218:221], v[140:141], v[180:181], v[218:221]
	v_mfma_f32_4x4x4_16b_bf16 v[222:225], v[144:145], v[180:181], v[222:225]
	v_mfma_f32_4x4x4_16b_bf16 v[226:229], v[148:149], v[180:181], v[226:229]
	v_mfma_f32_4x4x4_16b_bf16 v[230:233], v[152:153], v[180:181], v[230:233]
	s_mov_b32 s98, 0x22222222
	s_mov_b32 s99, 0x22222222
	s_mov_b32 s100, 0x44444444
	s_mov_b32 s101, 0x44444444
	s_mov_b32 vcc_lo, 0x88888888
	s_mov_b32 vcc_hi, 0x88888888
	s_nop 4
	v_cndmask_b32_e64 v161, v218, v219, s[98:99]
	v_cndmask_b32_e64 v161, v161, v220, s[100:101]
	v_cndmask_b32_e32 v161, v161, v221, vcc
	v_cndmask_b32_e64 v162, v222, v223, s[98:99]
	v_cndmask_b32_e64 v162, v162, v224, s[100:101]
	v_cndmask_b32_e32 v162, v162, v225, vcc
	v_cndmask_b32_e64 v163, v226, v227, s[98:99]
	v_cndmask_b32_e64 v163, v163, v228, s[100:101]
	v_cndmask_b32_e32 v163, v163, v229, vcc
	v_cndmask_b32_e64 v164, v230, v231, s[98:99]
	v_cndmask_b32_e64 v164, v164, v232, s[100:101]
	v_cndmask_b32_e32 v164, v164, v233, vcc
	s_nop 1
	v_permlane32_swap_b32_e32 v88, v125
	v_permlane32_swap_b32_e32 v93, v158
	v_permlane32_swap_b32_e32 v96, v159
	v_permlane32_swap_b32_e32 v97, v160
	v_permlane32_swap_b32_e32 v121, v161
	v_permlane32_swap_b32_e32 v123, v162
	v_permlane32_swap_b32_e32 v124, v163
	v_permlane32_swap_b32_e32 v122, v164
	v_add_f32_e32 v86, v88, v125
	v_add_f32_e32 v87, v93, v158
	v_add_f32_e32 v88, v96, v159
	v_add_f32_e32 v89, v97, v160
	v_add_f32_e32 v90, v121, v161
	v_add_f32_e32 v91, v123, v162
	v_add_f32_e32 v92, v124, v163
	v_add_f32_e32 v93, v122, v164
	s_nop 1
	v_permlane16_swap_b32_e32 v86, v90
	v_permlane16_swap_b32_e32 v87, v91
	v_permlane16_swap_b32_e32 v88, v92
	v_permlane16_swap_b32_e32 v89, v93
	v_add_f32_e32 v86, v86, v90
	v_add_f32_e32 v87, v87, v91
	v_add_f32_e32 v88, v88, v92
	v_add_f32_e32 v89, v89, v93
	v_cndmask_b32_e64 v90, v86, v88, s[8:9]
	v_cndmask_b32_e64 v91, v87, v89, s[8:9]
	v_cndmask_b32_e64 v86, v88, v86, s[8:9]
	v_cndmask_b32_e64 v87, v89, v87, s[8:9]
	s_nop 0
	v_add_f32_dpp v86, v90, v86 row_ror:8 row_mask:0xf bank_mask:0xf
	v_add_f32_dpp v87, v91, v87 row_ror:8 row_mask:0xf bank_mask:0xf
	v_cndmask_b32_e64 v88, v86, v87, s[10:11]
	v_cndmask_b32_e64 v86, v87, v86, s[10:11]
	s_nop 1
	v_mov_b32_dpp v89, v88 row_half_mirror row_mask:0xf bank_mask:0xf
	s_nop 1
	v_add_f32_dpp v86, v89, v86 quad_perm:[3,2,1,0] row_mask:0xf bank_mask:0xf
	s_nop 1
	v_add_f32_dpp v87, v86, v86 quad_perm:[2,3,0,1] row_mask:0xf bank_mask:0xf
	s_nop 1
	v_add_f32_dpp v86, v87, v87 quad_perm:[1,0,3,2] row_mask:0xf bank_mask:0xf
	s_nop 1
	v_mov_b32_dpp v88, v86 row_half_mirror row_mask:0xf bank_mask:0xf
	s_nop 1
	v_max_f32_dpp v87, v88, v86 quad_perm:[3,2,1,0] row_mask:0xf bank_mask:0xf
	s_nop 1
	v_max_f32_dpp v88, v87, v87 row_ror:8 row_mask:0xf bank_mask:0xf
	v_mov_b32_e32 v87, v88
	s_nop 1
	v_permlane16_swap_b32_e32 v88, v87
	v_max_f32_e32 v87, v88, v87
	v_mov_b32_e32 v88, v87
	s_nop 1
	v_permlane32_swap_b32_e32 v87, v88
	v_max_f32_e32 v87, v87, v88
	v_sub_f32_e32 v86, v86, v87
	v_mul_f32_e32 v86, 0x3fb8aa3b, v86
	v_exp_f32_e32 v86, v86
	s_nop 1
	v_mov_b32_dpp v88, v86 row_half_mirror row_mask:0xf bank_mask:0xf
	s_nop 1
	v_add_f32_dpp v87, v88, v86 quad_perm:[3,2,1,0] row_mask:0xf bank_mask:0xf
	s_nop 1
	v_add_f32_dpp v88, v87, v87 row_ror:8 row_mask:0xf bank_mask:0xf
	v_mov_b32_e32 v87, v88
	s_nop 1
	v_permlane16_swap_b32_e32 v88, v87
	v_add_f32_e32 v87, v88, v87
	v_mov_b32_e32 v88, v87
	s_nop 1
	v_permlane32_swap_b32_e32 v87, v88
	v_add_f32_e32 v87, v87, v88
	s_and_saveexec_b64 s[0:1], s[12:13]
	s_cbranch_execz .LBB0_1935
	s_waitcnt lgkmcnt(0)
	s_nop 0
	v_div_scale_f32 v88, s[14:15], v87, v87, v86
	v_rcp_f32_e32 v89, v88
	v_div_scale_f32 v90, vcc, v86, v87, v86
	s_and_b32 s14, s16, 0x7ff
	v_fma_f32 v91, -v88, v89, 1.0
	v_fmac_f32_e32 v89, v91, v89
	v_mul_f32_e32 v91, v90, v89
	v_fma_f32 v92, -v88, v91, v90
	v_fmac_f32_e32 v91, v92, v89
	v_fma_f32 v88, -v88, v91, v90
	v_div_fmas_f32 v88, v88, v89, v91
	v_div_fixup_f32 v88, v88, v87, v86
	v_lshl_or_b32 v86, s18, 4, v108
	v_ashrrev_i32_e32 v87, 31, v86
	v_lshlrev_b64 v[86:87], 13, v[86:87]
	v_lshl_add_u64 v[86:87], s[20:21], 0, v[86:87]
	s_lshl_b32 s18, s14, 2
	v_lshl_add_u64 v[86:87], v[86:87], 0, s[18:19]
	global_store_dword v[86:87], v88, off
	s_branch .LBB0_1935

; template <int LO, int HI>
; __global__ void __launch_bounds__(NWAVES * 64, 2) trunk_fwd(Args args) {
	.amdhsa_kernel _Z9trunk_fwdILi0ELi24EEv4Args
		.amdhsa_group_segment_fixed_size 0
		.amdhsa_private_segment_fixed_size 0
		.amdhsa_kernarg_size 488
		.amdhsa_user_sgpr_count 2
		.amdhsa_user_sgpr_dispatch_ptr 0
		.amdhsa_user_sgpr_queue_ptr 0
		.amdhsa_user_sgpr_kernarg_segment_ptr 1
		.amdhsa_user_sgpr_dispatch_id 0
		.amdhsa_user_sgpr_kernarg_preload_length 0
		.amdhsa_user_sgpr_kernarg_preload_offset 0
		.amdhsa_user_sgpr_private_segment_size 0
		.amdhsa_uses_dynamic_stack 0
		.amdhsa_enable_private_segment 0
		.amdhsa_system_sgpr_workgroup_id_x 1
		.amdhsa_system_sgpr_workgroup_id_y 0
		.amdhsa_system_sgpr_workgroup_id_z 0
		.amdhsa_system_sgpr_workgroup_info 0
		.amdhsa_system_vgpr_workitem_id 0
		.amdhsa_next_free_vgpr 250
		.amdhsa_next_free_sgpr 102
		.amdhsa_accum_offset 252
		.amdhsa_reserve_vcc 1
		.amdhsa_float_round_mode_32 0
		.amdhsa_float_round_mode_16_64 0
		.amdhsa_float_denorm_mode_32 3
		.amdhsa_float_denorm_mode_16_64 3
		.amdhsa_dx10_clamp 1
		.amdhsa_ieee_mode 1
		.amdhsa_fp16_overflow 0
		.amdhsa_tg_split 0
		.amdhsa_exception_fp_ieee_invalid_op 0
		.amdhsa_exception_fp_denorm_src 0
		.amdhsa_exception_fp_ieee_div_zero 0
		.amdhsa_exception_fp_ieee_overflow 0
		.amdhsa_exception_fp_ieee_underflow 0
		.amdhsa_exception_fp_ieee_inexact 0
		.amdhsa_exception_int_div_zero 0
	.end_amdhsa_kernel

; template <int LO, int HI>
; __global__ void __launch_bounds__(NWAVES * 64, 2) trunk_fwd(Args args) {
amdhsa.kernels:
  - .agpr_count:     0
    .args:
      - .offset:         0
        .size:           232
        .value_kind:     by_value
      - .offset:         232
        .size:           4
        .value_kind:     hidden_block_count_x
      - .offset:         236
        .size:           4
        .value_kind:     hidden_block_count_y
      - .offset:         240
        .size:           4
        .value_kind:     hidden_block_count_z
      - .offset:         244
        .size:           2
        .value_kind:     hidden_group_size_x
      - .offset:         246
        .size:           2
        .value_kind:     hidden_group_size_y
      - .offset:         248
        .size:           2
        .value_kind:     hidden_group_size_z
      - .offset:         250
        .size:           2
        .value_kind:     hidden_remainder_x
      - .offset:         252
        .size:           2
        .value_kind:     hidden_remainder_y
      - .offset:         254
        .size:           2
        .value_kind:     hidden_remainder_z
      - .offset:         272
        .size:           8
        .value_kind:     hidden_global_offset_x
      - .offset:         280
        .size:           8
        .value_kind:     hidden_global_offset_y
      - .offset:         288
        .size:           8
        .value_kind:     hidden_global_offset_z
      - .offset:         296
        .size:           2
        .value_kind:     hidden_grid_dims
      - .offset:         352
        .size:           4
        .value_kind:     hidden_dynamic_lds_size
    .group_segment_fixed_size: 0
    .kernarg_segment_align: 8
    .kernarg_segment_size: 488
    .language:       OpenCL C
    .language_version:
      - 2
      - 0
    .max_flat_workgroup_size: 512
    .name:           _Z9trunk_fwdILi0ELi24EEv4Args
    .private_segment_fixed_size: 0
    .sgpr_count:     108
    .sgpr_spill_count: 30
    .symbol:         _Z9trunk_fwdILi0ELi24EEv4Args.kd
    .uniform_work_group_size: 1
    .uses_dynamic_stack: false
    .vgpr_count:     250
    .vgpr_spill_count: 0
    .wavefront_size: 64
